# less VALU per MFMA (docs 9.3 DVFS note): t+3 stage addresses via instruction offset:128 instead of 54 64-bit VALU adds, on top of one priority raise per MFMA segment
# speedup vs baseline: 1.0038x; 1.0038x over previous
; #define PG8_STAGE(bufoff, gbase, voff) do { _Pragma("unroll") for (int _i = 0; _i < 2; ++_i) \
;         __builtin_amdgcn_global_load_lds((const unsigned*)((const char*)(gbase) + (voff)[_i]), (PG8_LAS unsigned*)(lds + (bufoff) + ldsw + _i * 8192), 16, 0, 0); } while (0)
; #define PG8_LDA(dst, b, h) do { _Pragma("unroll") for (int m = 0; m < 4; ++m) { const bf16x8 f0_ = *(const PG8_LAS bf16x8*)(lds + PG8_SA(b, h) + aoff + m * 2048), f1_ = *(const PG8_LAS bf16x8*)(lds + PG8_SA(b, h) + aoff + m * 2048 + 1024); dst[m].set(f0_, f1_); } } while (0)
; #define PG8_LDB(dst, b, h) do { _Pragma("unroll") for (int n = 0; n < 2; ++n) { const bf16x8 f0_ = *(const PG8_LAS bf16x8*)(lds + PG8_SB(b, h) + boff + n * 2048), f1_ = *(const PG8_LAS bf16x8*)(lds + PG8_SB(b, h) + boff + n * 2048 + 1024); dst[n].set(f0_, f1_); } } while (0)
; #define PG8_WAIT_V(n) asm volatile("s_waitcnt vmcnt(" #n ")" ::: "memory")
; #define PG8_WAIT_L(n) asm volatile("s_waitcnt lgkmcnt(" #n ")" ::: "memory")
; #define PG8_BAR __builtin_amdgcn_s_barrier()
; #define PG8_SCHED __builtin_amdgcn_sched_barrier(0)
; template <class Epi, class Sched, bool ALIGN_EPI = false, bool SP2 = false>
; __device__ __forceinline__ void gemm_phase(PG8_LAS unsigned char* lds, const Gemm g, const Sched& S, const Epi& E) {
;     ...
;             PG8_LDB(B0, 0, 0); PG8_LDB(B1, 0, 1); PG8_SCHED; PG8_LDA(At, 0, 0); PG8_STAGE(PG8_SA(1, 1), a1 + hstep, voffA);
;             PG8_WAIT_V(8); PG8_WAIT_L(0); PG8_BAR; PG8_MMA(0, 0, At, B0); PG8_MMA(0, 1, At, B1); PG8_BAR; PG8_SCHED;
;             PG8_LDA(At, 0, 1); PG8_STAGE(PG8_SB(0, 0), b2, voffB); PG8_STAGE(PG8_SB(0, 1), b2 + hstepB, voffB); PG8_STAGE(PG8_SA(0, 0), a2, voffA);
;             PG8_WAIT_V(8); PG8_WAIT_L(0); PG8_BAR; PG8_MMA(1, 0, At, B0); PG8_MMA(1, 1, At, B1); PG8_BAR; PG8_SCHED;
.Lkr0_a:
	v_lshl_add_u64 v[190:191], s[2:3], 0, v[174:175]
	s_add_i32 m0, s58, 0xc000
	ds_read_b128 v[182:185], v205
	ds_read_b128 v[186:189], v205 offset:1024
	ds_read_b128 v[212:215], v205 offset:2048
	ds_read_b128 v[216:219], v205 offset:3072
	ds_read_b128 v[220:223], v205 offset:4096
	ds_read_b128 v[224:227], v205 offset:5120
	ds_read_b128 v[228:231], v205 offset:6144
	ds_read_b128 v[232:235], v205 offset:7168
	global_load_lds_dwordx4 v[190:191], off
	v_lshl_add_u64 v[190:191], s[2:3], 0, v[176:177]
	s_add_i32 m0, s58, 0xe000
	s_nop 0
	global_load_lds_dwordx4 v[190:191], off
	s_waitcnt vmcnt(8)
	s_waitcnt lgkmcnt(0)
	s_barrier
	s_setprio 1
	s_waitcnt lgkmcnt(0)
	v_mfma_scale_f32_16x16x128_f8f6f4 v[158:161], v[18:25], v[182:189], v[158:161], v206, v207 op_sel_hi:[0,0,0]
	v_mfma_scale_f32_16x16x128_f8f6f4 v[154:157], v[26:33], v[182:189], v[154:157], v206, v207 op_sel_hi:[0,0,0]
	v_mfma_scale_f32_16x16x128_f8f6f4 v[142:145], v[18:25], v[212:219], v[142:145], v206, v207 op_sel_hi:[0,0,0]
	v_mfma_scale_f32_16x16x128_f8f6f4 v[138:141], v[26:33], v[212:219], v[138:141], v206, v207 op_sel_hi:[0,0,0]
	v_mfma_scale_f32_16x16x128_f8f6f4 v[126:129], v[18:25], v[220:227], v[126:129], v206, v207 op_sel_hi:[0,0,0]
	v_mfma_scale_f32_16x16x128_f8f6f4 v[122:125], v[26:33], v[220:227], v[122:125], v206, v207 op_sel_hi:[0,0,0]
	v_mfma_scale_f32_16x16x128_f8f6f4 v[110:113], v[18:25], v[228:235], v[110:113], v206, v207 op_sel_hi:[0,0,0]
	v_mfma_scale_f32_16x16x128_f8f6f4 v[106:109], v[26:33], v[228:235], v[106:109], v206, v207 op_sel_hi:[0,0,0]
	v_mfma_scale_f32_16x16x128_f8f6f4 v[150:153], v[2:9], v[182:189], v[150:153], v206, v207 op_sel_hi:[0,0,0]
	v_mfma_scale_f32_16x16x128_f8f6f4 v[146:149], v[10:17], v[182:189], v[146:149], v206, v207 op_sel_hi:[0,0,0]
	v_mfma_scale_f32_16x16x128_f8f6f4 v[134:137], v[2:9], v[212:219], v[134:137], v206, v207 op_sel_hi:[0,0,0]
	v_mfma_scale_f32_16x16x128_f8f6f4 v[130:133], v[10:17], v[212:219], v[130:133], v206, v207 op_sel_hi:[0,0,0]
	v_mfma_scale_f32_16x16x128_f8f6f4 v[118:121], v[2:9], v[220:227], v[118:121], v206, v207 op_sel_hi:[0,0,0]
	v_mfma_scale_f32_16x16x128_f8f6f4 v[114:117], v[10:17], v[220:227], v[114:117], v206, v207 op_sel_hi:[0,0,0]
	v_mfma_scale_f32_16x16x128_f8f6f4 v[102:105], v[2:9], v[228:235], v[102:105], v206, v207 op_sel_hi:[0,0,0]
	v_mfma_scale_f32_16x16x128_f8f6f4 v[98:101], v[10:17], v[228:235], v[98:101], v206, v207 op_sel_hi:[0,0,0]
	s_setprio 0
	s_barrier
	s_add_i32 s0, s76, s57
	v_lshl_add_u64 v[182:183], s[50:51], 0, v[164:165]
	s_mov_b32 m0, s0
	ds_read_b128 v[212:215], v205 offset:16384
	ds_read_b128 v[216:219], v205 offset:17408
	ds_read_b128 v[220:223], v205 offset:18432
	ds_read_b128 v[224:227], v205 offset:19456
	ds_read_b128 v[228:231], v205 offset:20480
	ds_read_b128 v[232:235], v205 offset:21504
	ds_read_b128 v[236:239], v205 offset:22528
	ds_read_b128 v[240:243], v205 offset:23552
	global_load_lds_dwordx4 v[182:183], off
	s_add_i32 m0, s0, 0x2000
	v_lshl_add_u64 v[184:185], s[50:51], 0, v[168:169]
	s_add_u32 s50, s50, s16
	s_addc_u32 s51, s51, s17
	s_add_i32 s0, s77, s57
	global_load_lds_dwordx4 v[184:185], off
	v_lshl_add_u64 v[186:187], s[50:51], 0, v[164:165]
	s_mov_b32 m0, s0
	v_lshl_add_u64 v[188:189], s[50:51], 0, v[168:169]
	global_load_lds_dwordx4 v[186:187], off
	s_add_i32 m0, s0, 0x2000
	v_lshl_add_u64 v[190:191], s[48:49], 0, v[162:163]
	global_load_lds_dwordx4 v[188:189], off
	v_lshl_add_u64 v[192:193], s[48:49], 0, v[166:167]
	s_waitcnt vmcnt(6)
	s_waitcnt lgkmcnt(0)
	s_barrier
	s_setprio 1
	s_waitcnt lgkmcnt(0)
	v_mfma_scale_f32_16x16x128_f8f6f4 v[94:97], v[18:25], v[212:219], v[94:97], v206, v207 op_sel_hi:[0,0,0]
	v_mfma_scale_f32_16x16x128_f8f6f4 v[90:93], v[26:33], v[212:219], v[90:93], v206, v207 op_sel_hi:[0,0,0]
	v_mfma_scale_f32_16x16x128_f8f6f4 v[78:81], v[18:25], v[220:227], v[78:81], v206, v207 op_sel_hi:[0,0,0]
	v_mfma_scale_f32_16x16x128_f8f6f4 v[74:77], v[26:33], v[220:227], v[74:77], v206, v207 op_sel_hi:[0,0,0]
	v_mfma_scale_f32_16x16x128_f8f6f4 v[62:65], v[18:25], v[228:235], v[62:65], v206, v207 op_sel_hi:[0,0,0]
	v_mfma_scale_f32_16x16x128_f8f6f4 v[58:61], v[26:33], v[228:235], v[58:61], v206, v207 op_sel_hi:[0,0,0]
	v_mfma_scale_f32_16x16x128_f8f6f4 v[46:49], v[18:25], v[236:243], v[46:49], v206, v207 op_sel_hi:[0,0,0]
	v_mfma_scale_f32_16x16x128_f8f6f4 v[42:45], v[26:33], v[236:243], v[42:45], v206, v207 op_sel_hi:[0,0,0]
	v_mfma_scale_f32_16x16x128_f8f6f4 v[86:89], v[2:9], v[212:219], v[86:89], v206, v207 op_sel_hi:[0,0,0]
	v_mfma_scale_f32_16x16x128_f8f6f4 v[82:85], v[10:17], v[212:219], v[82:85], v206, v207 op_sel_hi:[0,0,0]
	v_mfma_scale_f32_16x16x128_f8f6f4 v[70:73], v[2:9], v[220:227], v[70:73], v206, v207 op_sel_hi:[0,0,0]
	v_mfma_scale_f32_16x16x128_f8f6f4 v[66:69], v[10:17], v[220:227], v[66:69], v206, v207 op_sel_hi:[0,0,0]
	v_mfma_scale_f32_16x16x128_f8f6f4 v[54:57], v[2:9], v[228:235], v[54:57], v206, v207 op_sel_hi:[0,0,0]
	v_mfma_scale_f32_16x16x128_f8f6f4 v[50:53], v[10:17], v[228:235], v[50:53], v206, v207 op_sel_hi:[0,0,0]
	v_mfma_scale_f32_16x16x128_f8f6f4 v[38:41], v[2:9], v[236:243], v[38:41], v206, v207 op_sel_hi:[0,0,0]
	v_mfma_scale_f32_16x16x128_f8f6f4 v[34:37], v[10:17], v[236:243], v[34:37], v206, v207 op_sel_hi:[0,0,0]
	s_setprio 0
	s_barrier
; #define PG8_STAGE(bufoff, gbase, voff) do { _Pragma("unroll") for (int _i = 0; _i < 2; ++_i) \
;         __builtin_amdgcn_global_load_lds((const unsigned*)((const char*)(gbase) + (voff)[_i]), (PG8_LAS unsigned*)(lds + (bufoff) + ldsw + _i * 8192), 16, 0, 0); } while (0)
; #define PG8_LDA(dst, b, h) do { _Pragma("unroll") for (int m = 0; m < 4; ++m) { const bf16x8 f0_ = *(const PG8_LAS bf16x8*)(lds + PG8_SA(b, h) + aoff + m * 2048), f1_ = *(const PG8_LAS bf16x8*)(lds + PG8_SA(b, h) + aoff + m * 2048 + 1024); dst[m].set(f0_, f1_); } } while (0)
; #define PG8_LDB(dst, b, h) do { _Pragma("unroll") for (int n = 0; n < 2; ++n) { const bf16x8 f0_ = *(const PG8_LAS bf16x8*)(lds + PG8_SB(b, h) + boff + n * 2048), f1_ = *(const PG8_LAS bf16x8*)(lds + PG8_SB(b, h) + boff + n * 2048 + 1024); dst[n].set(f0_, f1_); } } while (0)
; #define PG8_WAIT_V(n) asm volatile("s_waitcnt vmcnt(" #n ")" ::: "memory")
; #define PG8_WAIT_L(n) asm volatile("s_waitcnt lgkmcnt(" #n ")" ::: "memory")
; #define PG8_BAR __builtin_amdgcn_s_barrier()
; #define PG8_SCHED __builtin_amdgcn_sched_barrier(0)
; template <class Epi, class Sched, bool ALIGN_EPI = false, bool SP2 = false>
; __device__ __forceinline__ void gemm_phase(PG8_LAS unsigned char* lds, const Gemm g, const Sched& S, const Epi& E) {
;     ...
;             PG8_LDB(B0, 1, 0); PG8_LDB(B1, 1, 1); PG8_SCHED; PG8_LDA(At, 1, 0); PG8_STAGE(PG8_SA(0, 1), a2 + hstep, voffA);
;             PG8_WAIT_V(8); PG8_WAIT_L(0); PG8_BAR; PG8_MMA(0, 0, At, B0); PG8_MMA(0, 1, At, B1); PG8_BAR; PG8_SCHED;
;             PG8_LDA(At, 1, 1); PG8_STAGE(PG8_SB(1, 0), b3, voffB); PG8_STAGE(PG8_SB(1, 1), b3 + hstepB, voffB); PG8_STAGE(PG8_SA(1, 0), a3, voffA);
	s_add_i32 s0, 0, 0x18000
	s_add_i32 s1, 0, 0x1c000
	v_add_u32_e32 v14, s0, v194
	v_add_u32_e32 v30, s1, v194
	ds_read_b128 v[2:5], v14
	ds_read_b128 v[6:9], v14 offset:1024
	ds_read_b128 v[10:13], v14 offset:2048
	ds_read_b128 v[14:17], v14 offset:3072
	ds_read_b128 v[18:21], v30
	ds_read_b128 v[22:25], v30 offset:1024
	ds_read_b128 v[26:29], v30 offset:2048
	ds_read_b128 v[30:33], v30 offset:3072
	s_add_u32 s48, s48, s14
	s_addc_u32 s49, s49, s15
	s_mov_b32 m0, s61
	v_lshl_add_u64 v[244:245], s[48:49], 0, v[162:163]
	ds_read_b128 v[212:215], v205 offset:32768
	ds_read_b128 v[216:219], v205 offset:33792
	ds_read_b128 v[220:223], v205 offset:34816
	ds_read_b128 v[224:227], v205 offset:35840
	ds_read_b128 v[228:231], v205 offset:36864
	ds_read_b128 v[232:235], v205 offset:37888
	ds_read_b128 v[236:239], v205 offset:38912
	ds_read_b128 v[240:243], v205 offset:39936
	s_mov_b32 m0, s58
	s_nop 0
	global_load_lds_dwordx4 v[190:191], off
	s_mov_b32 m0, s59
	s_nop 0
	global_load_lds_dwordx4 v[192:193], off
	s_mov_b32 m0, s61
	s_nop 0
	global_load_lds_dwordx4 v[244:245], off
	v_lshl_add_u64 v[244:245], s[48:49], 0, v[166:167]
	s_mov_b32 m0, s63
	s_nop 0
	global_load_lds_dwordx4 v[244:245], off
	s_waitcnt vmcnt(8)
	s_waitcnt lgkmcnt(0)
	s_barrier
	s_setprio 1
	s_waitcnt lgkmcnt(0)
	v_mfma_scale_f32_16x16x128_f8f6f4 v[158:161], v[2:9], v[212:219], v[158:161], v206, v207 op_sel_hi:[0,0,0]
	v_mfma_scale_f32_16x16x128_f8f6f4 v[154:157], v[10:17], v[212:219], v[154:157], v206, v207 op_sel_hi:[0,0,0]
	v_mfma_scale_f32_16x16x128_f8f6f4 v[142:145], v[2:9], v[220:227], v[142:145], v206, v207 op_sel_hi:[0,0,0]
	v_mfma_scale_f32_16x16x128_f8f6f4 v[138:141], v[10:17], v[220:227], v[138:141], v206, v207 op_sel_hi:[0,0,0]
	v_mfma_scale_f32_16x16x128_f8f6f4 v[126:129], v[2:9], v[228:235], v[126:129], v206, v207 op_sel_hi:[0,0,0]
	v_mfma_scale_f32_16x16x128_f8f6f4 v[122:125], v[10:17], v[228:235], v[122:125], v206, v207 op_sel_hi:[0,0,0]
	v_mfma_scale_f32_16x16x128_f8f6f4 v[110:113], v[2:9], v[236:243], v[110:113], v206, v207 op_sel_hi:[0,0,0]
	v_mfma_scale_f32_16x16x128_f8f6f4 v[106:109], v[10:17], v[236:243], v[106:109], v206, v207 op_sel_hi:[0,0,0]
	v_mfma_scale_f32_16x16x128_f8f6f4 v[150:153], v[18:25], v[212:219], v[150:153], v206, v207 op_sel_hi:[0,0,0]
	v_mfma_scale_f32_16x16x128_f8f6f4 v[146:149], v[26:33], v[212:219], v[146:149], v206, v207 op_sel_hi:[0,0,0]
	v_mfma_scale_f32_16x16x128_f8f6f4 v[134:137], v[18:25], v[220:227], v[134:137], v206, v207 op_sel_hi:[0,0,0]
	v_mfma_scale_f32_16x16x128_f8f6f4 v[130:133], v[26:33], v[220:227], v[130:133], v206, v207 op_sel_hi:[0,0,0]
	v_mfma_scale_f32_16x16x128_f8f6f4 v[118:121], v[18:25], v[228:235], v[118:121], v206, v207 op_sel_hi:[0,0,0]
	v_mfma_scale_f32_16x16x128_f8f6f4 v[114:117], v[26:33], v[228:235], v[114:117], v206, v207 op_sel_hi:[0,0,0]
	v_mfma_scale_f32_16x16x128_f8f6f4 v[102:105], v[18:25], v[236:243], v[102:105], v206, v207 op_sel_hi:[0,0,0]
	v_mfma_scale_f32_16x16x128_f8f6f4 v[98:101], v[26:33], v[236:243], v[98:101], v206, v207 op_sel_hi:[0,0,0]
	s_setprio 0
	s_barrier
	s_add_i32 s0, s0, s57
	s_add_i32 m0, s0, 0xffffff80
	ds_read_b128 v[212:215], v205 offset:49152
	ds_read_b128 v[216:219], v205 offset:50176
	ds_read_b128 v[220:223], v205 offset:51200
	ds_read_b128 v[224:227], v205 offset:52224
	ds_read_b128 v[228:231], v205 offset:53248
	ds_read_b128 v[232:235], v205 offset:54272
	ds_read_b128 v[236:239], v205 offset:55296
	ds_read_b128 v[240:243], v205 offset:56320
	global_load_lds_dwordx4 v[182:183], off offset:128
	s_add_i32 m0, s0, 0x1f80
	s_add_i32 s0, s1, s57
	global_load_lds_dwordx4 v[184:185], off offset:128
	s_add_i32 m0, s0, 0xffffff80
	s_nop 0
	global_load_lds_dwordx4 v[186:187], off offset:128
	s_add_i32 m0, s0, 0x1f80
	s_nop 0
	global_load_lds_dwordx4 v[188:189], off offset:128
	s_cmp_ge_i32 s53, s69
	s_cbranch_scc0 .Lkr0_b
	s_add_i32 m0, s66, 0xffffff80
	s_nop 0
	global_load_lds_dwordx4 v[190:191], off offset:128
	s_add_i32 m0, s67, 0xffffff80
	s_nop 0
	global_load_lds_dwordx4 v[192:193], off offset:128

; #define PG8_STAGE(bufoff, gbase, voff) do { _Pragma("unroll") for (int _i = 0; _i < 2; ++_i) \
;         __builtin_amdgcn_global_load_lds((const unsigned*)((const char*)(gbase) + (voff)[_i]), (PG8_LAS unsigned*)(lds + (bufoff) + ldsw + _i * 8192), 16, 0, 0); } while (0)
; #define PG8_LDA(dst, b, h) do { _Pragma("unroll") for (int m = 0; m < 4; ++m) { const bf16x8 f0_ = *(const PG8_LAS bf16x8*)(lds + PG8_SA(b, h) + aoff + m * 2048), f1_ = *(const PG8_LAS bf16x8*)(lds + PG8_SA(b, h) + aoff + m * 2048 + 1024); dst[m].set(f0_, f1_); } } while (0)
; #define PG8_LDB(dst, b, h) do { _Pragma("unroll") for (int n = 0; n < 2; ++n) { const bf16x8 f0_ = *(const PG8_LAS bf16x8*)(lds + PG8_SB(b, h) + boff + n * 2048), f1_ = *(const PG8_LAS bf16x8*)(lds + PG8_SB(b, h) + boff + n * 2048 + 1024); dst[n].set(f0_, f1_); } } while (0)
; #define PG8_WAIT_V(n) asm volatile("s_waitcnt vmcnt(" #n ")" ::: "memory")
; #define PG8_WAIT_L(n) asm volatile("s_waitcnt lgkmcnt(" #n ")" ::: "memory")
; #define PG8_BAR __builtin_amdgcn_s_barrier()
; #define PG8_SCHED __builtin_amdgcn_sched_barrier(0)
; template <class Epi, class Sched, bool ALIGN_EPI = false, bool SP2 = false>
; __device__ __forceinline__ void gemm_phase(PG8_LAS unsigned char* lds, const Gemm g, const Sched& S, const Epi& E) {
;     ...
;             const bool last = (t == nt - 2);
;             const char* a1 = cA + (size_t)(t + 1) * kstep;
;             const char* a2 = last ? nA : cA + (size_t)(t + 2) * kstep; const char* b2 = last ? nB : cB + (size_t)(t + 2) * kstep;
;             const char* a3 = a2 + kstep; const char* b3 = b2 + kstep;
;             if (last && has_next) S.a_ready(nxt);
;             if constexpr (SP2) {
;             PG8_LDB(B0, 0, 0); PG8_LDB(B1, 0, 1); PG8_SCHED; PG8_LDA(At, 0, 0); PG8_STAGE(PG8_SA(1, 1), a1 + hstep, voffA);
;             PG8_WAIT_V(8); PG8_WAIT_L(0); PG8_BAR; PG8_MMA(0, 0, At, B0); PG8_MMA(0, 1, At, B1); PG8_BAR; PG8_SCHED;
;             PG8_LDA(At, 0, 1); PG8_STAGE(PG8_SB(0, 0), b2, voffB); PG8_STAGE(PG8_SB(0, 1), b2 + hstepB, voffB); PG8_STAGE(PG8_SA(0, 0), a2, voffA);
;             PG8_WAIT_V(8); PG8_WAIT_L(0); PG8_BAR; PG8_MMA(1, 0, At, B0); PG8_MMA(1, 1, At, B1); PG8_BAR; PG8_SCHED;
.LBB0_984:
	s_add_i32 s75, s42, 2
	v_add_u32_e32 v186, s59, v173
	v_add_u32_e32 v202, s61, v173
	s_add_u32 s0, s38, s40
	ds_read_b128 v[168:171], v186
	ds_read_b128 v[178:181], v186 offset:1024
	ds_read_b128 v[182:185], v186 offset:2048
	ds_read_b128 v[186:189], v186 offset:3072
	ds_read_b128 v[190:193], v202
	ds_read_b128 v[194:197], v202 offset:1024
	ds_read_b128 v[198:201], v202 offset:2048
	ds_read_b128 v[202:205], v202 offset:3072
	s_addc_u32 s1, s39, s41
	s_add_u32 s0, s0, 0x100
	s_addc_u32 s1, s1, 0
	s_add_u32 s33, s73, s40
	s_addc_u32 s76, s74, s41
	s_cmp_eq_u32 s57, s42
	s_cselect_b32 s43, s3, s1
	s_cselect_b32 s42, s2, s0
	s_cselect_b32 s1, s37, s76
	s_cselect_b32 s0, s36, s33
	v_lshl_add_u64 v[240:241], v[164:165], 0, s[40:41]
	s_add_i32 m0, s47, 0xc000
	ds_read_b128 v[206:209], v176
	ds_read_b128 v[212:215], v176 offset:1024
	ds_read_b128 v[216:219], v176 offset:2048
	ds_read_b128 v[220:223], v176 offset:3072
	ds_read_b128 v[224:227], v176 offset:4096
	ds_read_b128 v[228:231], v176 offset:5120
	ds_read_b128 v[232:235], v176 offset:6144
	ds_read_b128 v[236:239], v176 offset:7168
	global_load_lds_dwordx4 v[240:241], off
	v_lshl_add_u64 v[240:241], v[166:167], 0, s[40:41]
	s_add_i32 m0, s47, 0xe000
	s_nop 0
	global_load_lds_dwordx4 v[240:241], off
	s_waitcnt vmcnt(8)
	s_waitcnt lgkmcnt(0)
	s_barrier
	s_setprio 1
	s_waitcnt lgkmcnt(0)
	v_mfma_f32_16x16x32_bf16 v[126:129], v[168:171], v[206:209], v[126:129]
	v_mfma_f32_16x16x32_bf16 v[122:125], v[182:185], v[206:209], v[122:125]
	v_mfma_f32_16x16x32_bf16 v[110:113], v[168:171], v[216:219], v[110:113]
	v_mfma_f32_16x16x32_bf16 v[106:109], v[182:185], v[216:219], v[106:109]
	v_mfma_f32_16x16x32_bf16 v[94:97], v[168:171], v[224:227], v[94:97]
	v_mfma_f32_16x16x32_bf16 v[90:93], v[182:185], v[224:227], v[90:93]
	v_mfma_f32_16x16x32_bf16 v[78:81], v[168:171], v[232:235], v[78:81]
	v_mfma_f32_16x16x32_bf16 v[74:77], v[182:185], v[232:235], v[74:77]
	v_mfma_f32_16x16x32_bf16 v[126:129], v[178:181], v[212:215], v[126:129]
	v_mfma_f32_16x16x32_bf16 v[122:125], v[186:189], v[212:215], v[122:125]
	v_mfma_f32_16x16x32_bf16 v[110:113], v[178:181], v[220:223], v[110:113]
	v_mfma_f32_16x16x32_bf16 v[106:109], v[186:189], v[220:223], v[106:109]
	v_mfma_f32_16x16x32_bf16 v[94:97], v[178:181], v[228:231], v[94:97]
	v_mfma_f32_16x16x32_bf16 v[90:93], v[186:189], v[228:231], v[90:93]
	v_mfma_f32_16x16x32_bf16 v[78:81], v[178:181], v[236:239], v[78:81]
	v_mfma_f32_16x16x32_bf16 v[74:77], v[186:189], v[236:239], v[74:77]
	v_mfma_f32_16x16x32_bf16 v[118:121], v[190:193], v[206:209], v[118:121]
	v_mfma_f32_16x16x32_bf16 v[114:117], v[198:201], v[206:209], v[114:117]
	v_mfma_f32_16x16x32_bf16 v[102:105], v[190:193], v[216:219], v[102:105]
	v_mfma_f32_16x16x32_bf16 v[98:101], v[198:201], v[216:219], v[98:101]
	v_mfma_f32_16x16x32_bf16 v[86:89], v[190:193], v[224:227], v[86:89]
	v_mfma_f32_16x16x32_bf16 v[82:85], v[198:201], v[224:227], v[82:85]
	v_mfma_f32_16x16x32_bf16 v[70:73], v[190:193], v[232:235], v[70:73]
	v_mfma_f32_16x16x32_bf16 v[66:69], v[198:201], v[232:235], v[66:69]
	v_mfma_f32_16x16x32_bf16 v[118:121], v[194:197], v[212:215], v[118:121]
	v_mfma_f32_16x16x32_bf16 v[114:117], v[202:205], v[212:215], v[114:117]
	v_mfma_f32_16x16x32_bf16 v[102:105], v[194:197], v[220:223], v[102:105]
	v_mfma_f32_16x16x32_bf16 v[98:101], v[202:205], v[220:223], v[98:101]
	v_mfma_f32_16x16x32_bf16 v[86:89], v[194:197], v[228:231], v[86:89]
	v_mfma_f32_16x16x32_bf16 v[82:85], v[202:205], v[228:231], v[82:85]
	v_mfma_f32_16x16x32_bf16 v[70:73], v[194:197], v[236:239], v[70:73]
	v_mfma_f32_16x16x32_bf16 v[66:69], v[202:205], v[236:239], v[66:69]
	s_setprio 0
	s_barrier
	s_add_i32 s33, s59, s46
	v_lshl_add_u64 v[240:241], s[0:1], 0, v[132:133]
	s_mov_b32 m0, s33
	ds_read_b128 v[206:209], v176 offset:16384
	ds_read_b128 v[212:215], v176 offset:17408
	ds_read_b128 v[216:219], v176 offset:18432
	ds_read_b128 v[220:223], v176 offset:19456
	ds_read_b128 v[224:227], v176 offset:20480
	ds_read_b128 v[228:231], v176 offset:21504
	ds_read_b128 v[232:235], v176 offset:22528
	ds_read_b128 v[236:239], v176 offset:23552
	global_load_lds_dwordx4 v[240:241], off
	s_add_i32 m0, s33, 0x2000
	v_lshl_add_u64 v[242:243], s[0:1], 0, v[136:137]
	s_add_u32 s0, s0, s14
	s_addc_u32 s1, s1, s15
	s_add_i32 s33, s61, s46
	global_load_lds_dwordx4 v[242:243], off
	v_lshl_add_u64 v[244:245], s[0:1], 0, v[132:133]
	s_mov_b32 m0, s33
	v_lshl_add_u64 v[246:247], s[0:1], 0, v[136:137]
	global_load_lds_dwordx4 v[244:245], off
	s_add_i32 m0, s33, 0x2000
	v_lshl_add_u64 v[248:249], s[42:43], 0, v[130:131]
	global_load_lds_dwordx4 v[246:247], off
	v_lshl_add_u64 v[250:251], s[42:43], 0, v[134:135]
	s_waitcnt vmcnt(6)
	s_waitcnt lgkmcnt(0)
	s_barrier
; #define PG8_STAGE(bufoff, gbase, voff) do { _Pragma("unroll") for (int _i = 0; _i < 2; ++_i) \
;         __builtin_amdgcn_global_load_lds((const unsigned*)((const char*)(gbase) + (voff)[_i]), (PG8_LAS unsigned*)(lds + (bufoff) + ldsw + _i * 8192), 16, 0, 0); } while (0)
; #define PG8_LDA(dst, b, h) do { _Pragma("unroll") for (int m = 0; m < 4; ++m) { const bf16x8 f0_ = *(const PG8_LAS bf16x8*)(lds + PG8_SA(b, h) + aoff + m * 2048), f1_ = *(const PG8_LAS bf16x8*)(lds + PG8_SA(b, h) + aoff + m * 2048 + 1024); dst[m].set(f0_, f1_); } } while (0)
; #define PG8_LDB(dst, b, h) do { _Pragma("unroll") for (int n = 0; n < 2; ++n) { const bf16x8 f0_ = *(const PG8_LAS bf16x8*)(lds + PG8_SB(b, h) + boff + n * 2048), f1_ = *(const PG8_LAS bf16x8*)(lds + PG8_SB(b, h) + boff + n * 2048 + 1024); dst[n].set(f0_, f1_); } } while (0)
; #define PG8_WAIT_V(n) asm volatile("s_waitcnt vmcnt(" #n ")" ::: "memory")
; #define PG8_WAIT_L(n) asm volatile("s_waitcnt lgkmcnt(" #n ")" ::: "memory")
; #define PG8_BAR __builtin_amdgcn_s_barrier()
; #define PG8_SCHED __builtin_amdgcn_sched_barrier(0)
; template <class Epi, class Sched, bool ALIGN_EPI = false, bool SP2 = false>
; __device__ __forceinline__ void gemm_phase(PG8_LAS unsigned char* lds, const Gemm g, const Sched& S, const Epi& E) {
;     ...
;             PG8_WAIT_V(8); PG8_WAIT_L(0); PG8_BAR; PG8_MMA(1, 0, At, B0); PG8_MMA(1, 1, At, B1); PG8_BAR; PG8_SCHED;
;             PG8_LDB(B0, 1, 0); PG8_LDB(B1, 1, 1); PG8_SCHED; PG8_LDA(At, 1, 0); PG8_STAGE(PG8_SA(0, 1), a2 + hstep, voffA);
;             PG8_WAIT_V(8); PG8_WAIT_L(0); PG8_BAR; PG8_MMA(0, 0, At, B0); PG8_MMA(0, 1, At, B1); PG8_BAR; PG8_SCHED;
	s_setprio 1
	s_waitcnt lgkmcnt(0)
	v_mfma_f32_16x16x32_bf16 v[62:65], v[168:171], v[206:209], v[62:65]
	v_mfma_f32_16x16x32_bf16 v[58:61], v[182:185], v[206:209], v[58:61]
	v_mfma_f32_16x16x32_bf16 v[46:49], v[168:171], v[216:219], v[46:49]
	v_mfma_f32_16x16x32_bf16 v[42:45], v[182:185], v[216:219], v[42:45]
	v_mfma_f32_16x16x32_bf16 v[30:33], v[168:171], v[224:227], v[30:33]
	v_mfma_f32_16x16x32_bf16 v[26:29], v[182:185], v[224:227], v[26:29]
	v_mfma_f32_16x16x32_bf16 v[14:17], v[168:171], v[232:235], v[14:17]
	v_mfma_f32_16x16x32_bf16 v[10:13], v[182:185], v[232:235], v[10:13]
	v_mfma_f32_16x16x32_bf16 v[62:65], v[178:181], v[212:215], v[62:65]
	v_mfma_f32_16x16x32_bf16 v[58:61], v[186:189], v[212:215], v[58:61]
	v_mfma_f32_16x16x32_bf16 v[46:49], v[178:181], v[220:223], v[46:49]
	v_mfma_f32_16x16x32_bf16 v[42:45], v[186:189], v[220:223], v[42:45]
	v_mfma_f32_16x16x32_bf16 v[30:33], v[178:181], v[228:231], v[30:33]
	v_mfma_f32_16x16x32_bf16 v[26:29], v[186:189], v[228:231], v[26:29]
	v_mfma_f32_16x16x32_bf16 v[14:17], v[178:181], v[236:239], v[14:17]
	v_mfma_f32_16x16x32_bf16 v[10:13], v[186:189], v[236:239], v[10:13]
	v_mfma_f32_16x16x32_bf16 v[54:57], v[190:193], v[206:209], v[54:57]
	v_mfma_f32_16x16x32_bf16 v[50:53], v[198:201], v[206:209], v[50:53]
	v_mfma_f32_16x16x32_bf16 v[38:41], v[190:193], v[216:219], v[38:41]
	v_mfma_f32_16x16x32_bf16 v[34:37], v[198:201], v[216:219], v[34:37]
	v_mfma_f32_16x16x32_bf16 v[22:25], v[190:193], v[224:227], v[22:25]
	v_mfma_f32_16x16x32_bf16 v[18:21], v[198:201], v[224:227], v[18:21]
	v_mfma_f32_16x16x32_bf16 v[6:9], v[190:193], v[232:235], v[6:9]
	v_mfma_f32_16x16x32_bf16 v[2:5], v[198:201], v[232:235], v[2:5]
	v_mfma_f32_16x16x32_bf16 v[54:57], v[194:197], v[212:215], v[54:57]
	v_mfma_f32_16x16x32_bf16 v[50:53], v[202:205], v[212:215], v[50:53]
	v_mfma_f32_16x16x32_bf16 v[38:41], v[194:197], v[220:223], v[38:41]
	v_mfma_f32_16x16x32_bf16 v[34:37], v[202:205], v[220:223], v[34:37]
	v_mfma_f32_16x16x32_bf16 v[22:25], v[194:197], v[228:231], v[22:25]
	v_mfma_f32_16x16x32_bf16 v[18:21], v[202:205], v[228:231], v[18:21]
	v_mfma_f32_16x16x32_bf16 v[6:9], v[194:197], v[236:239], v[6:9]
	v_mfma_f32_16x16x32_bf16 v[2:5], v[202:205], v[236:239], v[2:5]
	s_setprio 0
	s_barrier
	s_add_i32 s33, 0, 0x18000
	s_add_i32 s76, 0, 0x1c000
	v_add_u32_e32 v186, s33, v173
	v_add_u32_e32 v202, s76, v173
	ds_read_b128 v[168:171], v186
	ds_read_b128 v[178:181], v186 offset:1024
	ds_read_b128 v[182:185], v186 offset:2048
	ds_read_b128 v[186:189], v186 offset:3072
	ds_read_b128 v[190:193], v202
	ds_read_b128 v[194:197], v202 offset:1024
	ds_read_b128 v[198:201], v202 offset:2048
	ds_read_b128 v[202:205], v202 offset:3072
	s_add_u32 s0, s42, s12
	s_addc_u32 s1, s43, s13
	s_mov_b32 m0, s49
	v_lshl_add_u64 v[252:253], s[0:1], 0, v[130:131]
	ds_read_b128 v[206:209], v176 offset:32768
	ds_read_b128 v[212:215], v176 offset:33792
	ds_read_b128 v[216:219], v176 offset:34816
	ds_read_b128 v[220:223], v176 offset:35840
	ds_read_b128 v[224:227], v176 offset:36864
	ds_read_b128 v[228:231], v176 offset:37888
	ds_read_b128 v[232:235], v176 offset:38912
	ds_read_b128 v[236:239], v176 offset:39936
	s_mov_b32 m0, s47
	s_nop 0
	global_load_lds_dwordx4 v[248:249], off
	s_mov_b32 m0, s48
	s_nop 0
	global_load_lds_dwordx4 v[250:251], off
	s_mov_b32 m0, s49
	s_nop 0
	global_load_lds_dwordx4 v[252:253], off
	v_lshl_add_u64 v[252:253], s[0:1], 0, v[134:135]
	s_mov_b32 m0, s50
	s_nop 0
	global_load_lds_dwordx4 v[252:253], off
	s_waitcnt vmcnt(8)
	s_waitcnt lgkmcnt(0)
	s_barrier
; #define PG8_STAGE(bufoff, gbase, voff) do { _Pragma("unroll") for (int _i = 0; _i < 2; ++_i) \
;         __builtin_amdgcn_global_load_lds((const unsigned*)((const char*)(gbase) + (voff)[_i]), (PG8_LAS unsigned*)(lds + (bufoff) + ldsw + _i * 8192), 16, 0, 0); } while (0)
; #define PG8_LDA(dst, b, h) do { _Pragma("unroll") for (int m = 0; m < 4; ++m) { const bf16x8 f0_ = *(const PG8_LAS bf16x8*)(lds + PG8_SA(b, h) + aoff + m * 2048), f1_ = *(const PG8_LAS bf16x8*)(lds + PG8_SA(b, h) + aoff + m * 2048 + 1024); dst[m].set(f0_, f1_); } } while (0)
; #define PG8_WAIT_V(n) asm volatile("s_waitcnt vmcnt(" #n ")" ::: "memory")
; #define PG8_WAIT_L(n) asm volatile("s_waitcnt lgkmcnt(" #n ")" ::: "memory")
; #define PG8_BAR __builtin_amdgcn_s_barrier()
; #define PG8_SCHED __builtin_amdgcn_sched_barrier(0)
; template <class Epi, class Sched, bool ALIGN_EPI = false, bool SP2 = false>
; __device__ __forceinline__ void gemm_phase(PG8_LAS unsigned char* lds, const Gemm g, const Sched& S, const Epi& E) {
;     ...
;         for (int t = 0; t < nt; t += 2) {
;     ...
;             PG8_WAIT_V(8); PG8_WAIT_L(0); PG8_BAR; PG8_MMA(0, 0, At, B0); PG8_MMA(0, 1, At, B1); PG8_BAR; PG8_SCHED;
;             PG8_LDA(At, 1, 1); PG8_STAGE(PG8_SB(1, 0), b3, voffB); PG8_STAGE(PG8_SB(1, 1), b3 + hstepB, voffB); PG8_STAGE(PG8_SA(1, 0), a3, voffA);
;             PG8_WAIT_V(8); PG8_WAIT_L(0); PG8_BAR; PG8_MMA(1, 0, At, B0); PG8_MMA(1, 1, At, B1); PG8_BAR; PG8_SCHED;
	s_setprio 1
	s_waitcnt lgkmcnt(0)
	v_mfma_f32_16x16x32_bf16 v[126:129], v[168:171], v[206:209], v[126:129]
	v_mfma_f32_16x16x32_bf16 v[122:125], v[182:185], v[206:209], v[122:125]
	v_mfma_f32_16x16x32_bf16 v[110:113], v[168:171], v[216:219], v[110:113]
	v_mfma_f32_16x16x32_bf16 v[106:109], v[182:185], v[216:219], v[106:109]
	v_mfma_f32_16x16x32_bf16 v[94:97], v[168:171], v[224:227], v[94:97]
	v_mfma_f32_16x16x32_bf16 v[90:93], v[182:185], v[224:227], v[90:93]
	v_mfma_f32_16x16x32_bf16 v[78:81], v[168:171], v[232:235], v[78:81]
	v_mfma_f32_16x16x32_bf16 v[74:77], v[182:185], v[232:235], v[74:77]
	v_mfma_f32_16x16x32_bf16 v[126:129], v[178:181], v[212:215], v[126:129]
	v_mfma_f32_16x16x32_bf16 v[122:125], v[186:189], v[212:215], v[122:125]
	v_mfma_f32_16x16x32_bf16 v[110:113], v[178:181], v[220:223], v[110:113]
	v_mfma_f32_16x16x32_bf16 v[106:109], v[186:189], v[220:223], v[106:109]
	v_mfma_f32_16x16x32_bf16 v[94:97], v[178:181], v[228:231], v[94:97]
	v_mfma_f32_16x16x32_bf16 v[90:93], v[186:189], v[228:231], v[90:93]
	v_mfma_f32_16x16x32_bf16 v[78:81], v[178:181], v[236:239], v[78:81]
	v_mfma_f32_16x16x32_bf16 v[74:77], v[186:189], v[236:239], v[74:77]
	v_mfma_f32_16x16x32_bf16 v[118:121], v[190:193], v[206:209], v[118:121]
	v_mfma_f32_16x16x32_bf16 v[114:117], v[198:201], v[206:209], v[114:117]
	v_mfma_f32_16x16x32_bf16 v[102:105], v[190:193], v[216:219], v[102:105]
	v_mfma_f32_16x16x32_bf16 v[98:101], v[198:201], v[216:219], v[98:101]
	v_mfma_f32_16x16x32_bf16 v[86:89], v[190:193], v[224:227], v[86:89]
	v_mfma_f32_16x16x32_bf16 v[82:85], v[198:201], v[224:227], v[82:85]
	v_mfma_f32_16x16x32_bf16 v[70:73], v[190:193], v[232:235], v[70:73]
	v_mfma_f32_16x16x32_bf16 v[66:69], v[198:201], v[232:235], v[66:69]
	v_mfma_f32_16x16x32_bf16 v[118:121], v[194:197], v[212:215], v[118:121]
	v_mfma_f32_16x16x32_bf16 v[114:117], v[202:205], v[212:215], v[114:117]
	v_mfma_f32_16x16x32_bf16 v[102:105], v[194:197], v[220:223], v[102:105]
	v_mfma_f32_16x16x32_bf16 v[98:101], v[202:205], v[220:223], v[98:101]
	v_mfma_f32_16x16x32_bf16 v[86:89], v[194:197], v[228:231], v[86:89]
	v_mfma_f32_16x16x32_bf16 v[82:85], v[202:205], v[228:231], v[82:85]
	v_mfma_f32_16x16x32_bf16 v[70:73], v[194:197], v[236:239], v[70:73]
	v_mfma_f32_16x16x32_bf16 v[66:69], v[202:205], v[236:239], v[66:69]
	s_setprio 0
	s_barrier
	s_add_i32 s0, s33, s46
	s_add_i32 m0, s0, 0xffffff80
	ds_read_b128 v[206:209], v176 offset:49152
	ds_read_b128 v[212:215], v176 offset:50176
	ds_read_b128 v[216:219], v176 offset:51200
	ds_read_b128 v[220:223], v176 offset:52224
	ds_read_b128 v[224:227], v176 offset:53248
	ds_read_b128 v[228:231], v176 offset:54272
	ds_read_b128 v[232:235], v176 offset:55296
	ds_read_b128 v[236:239], v176 offset:56320
	global_load_lds_dwordx4 v[240:241], off offset:128
	s_add_i32 m0, s0, 0x1f80
	s_add_i32 s0, s76, s46
	global_load_lds_dwordx4 v[242:243], off offset:128
	s_add_i32 m0, s0, 0xffffff80
	s_nop 0
	global_load_lds_dwordx4 v[244:245], off offset:128
	s_add_i32 m0, s0, 0x1f80
	s_nop 0
	global_load_lds_dwordx4 v[246:247], off offset:128
	s_add_i32 m0, s52, 0xffffff80
	s_nop 0
	global_load_lds_dwordx4 v[248:249], off offset:128
	s_add_i32 m0, s53, 0xffffff80
	s_nop 0
	global_load_lds_dwordx4 v[250:251], off offset:128
	s_waitcnt vmcnt(6)
	s_waitcnt lgkmcnt(0)
	s_barrier
	s_setprio 1
	s_waitcnt lgkmcnt(0)
	v_mfma_f32_16x16x32_bf16 v[62:65], v[168:171], v[206:209], v[62:65]
	v_mfma_f32_16x16x32_bf16 v[58:61], v[182:185], v[206:209], v[58:61]
	v_mfma_f32_16x16x32_bf16 v[46:49], v[168:171], v[216:219], v[46:49]
	v_mfma_f32_16x16x32_bf16 v[42:45], v[182:185], v[216:219], v[42:45]
	v_mfma_f32_16x16x32_bf16 v[30:33], v[168:171], v[224:227], v[30:33]
	v_mfma_f32_16x16x32_bf16 v[26:29], v[182:185], v[224:227], v[26:29]
	v_mfma_f32_16x16x32_bf16 v[14:17], v[168:171], v[232:235], v[14:17]
	v_mfma_f32_16x16x32_bf16 v[10:13], v[182:185], v[232:235], v[10:13]
	v_mfma_f32_16x16x32_bf16 v[62:65], v[178:181], v[212:215], v[62:65]
	v_mfma_f32_16x16x32_bf16 v[58:61], v[186:189], v[212:215], v[58:61]
	v_mfma_f32_16x16x32_bf16 v[46:49], v[178:181], v[220:223], v[46:49]
	v_mfma_f32_16x16x32_bf16 v[42:45], v[186:189], v[220:223], v[42:45]
	v_mfma_f32_16x16x32_bf16 v[30:33], v[178:181], v[228:231], v[30:33]
	v_mfma_f32_16x16x32_bf16 v[26:29], v[186:189], v[228:231], v[26:29]
	v_mfma_f32_16x16x32_bf16 v[14:17], v[178:181], v[236:239], v[14:17]
	v_mfma_f32_16x16x32_bf16 v[10:13], v[186:189], v[236:239], v[10:13]
	v_mfma_f32_16x16x32_bf16 v[54:57], v[190:193], v[206:209], v[54:57]
	v_mfma_f32_16x16x32_bf16 v[50:53], v[198:201], v[206:209], v[50:53]
	v_mfma_f32_16x16x32_bf16 v[38:41], v[190:193], v[216:219], v[38:41]
	v_mfma_f32_16x16x32_bf16 v[34:37], v[198:201], v[216:219], v[34:37]
	v_mfma_f32_16x16x32_bf16 v[22:25], v[190:193], v[224:227], v[22:25]
	v_mfma_f32_16x16x32_bf16 v[18:21], v[198:201], v[224:227], v[18:21]
	v_mfma_f32_16x16x32_bf16 v[6:9], v[190:193], v[232:235], v[6:9]
	v_mfma_f32_16x16x32_bf16 v[2:5], v[198:201], v[232:235], v[2:5]
	v_mfma_f32_16x16x32_bf16 v[54:57], v[194:197], v[212:215], v[54:57]
	v_mfma_f32_16x16x32_bf16 v[50:53], v[202:205], v[212:215], v[50:53]
	v_mfma_f32_16x16x32_bf16 v[38:41], v[194:197], v[220:223], v[38:41]
	v_mfma_f32_16x16x32_bf16 v[34:37], v[202:205], v[220:223], v[34:37]
	v_mfma_f32_16x16x32_bf16 v[22:25], v[194:197], v[228:231], v[22:25]
	v_mfma_f32_16x16x32_bf16 v[18:21], v[202:205], v[228:231], v[18:21]
	v_mfma_f32_16x16x32_bf16 v[6:9], v[194:197], v[236:239], v[6:9]
	v_mfma_f32_16x16x32_bf16 v[2:5], v[202:205], v[236:239], v[2:5]
	s_setprio 0
	s_barrier
	s_add_u32 s40, s40, 0x100
	s_addc_u32 s41, s41, 0
	s_cmp_ge_i32 s75, s54
	s_cbranch_scc0 .LBB0_982

; #define PG8_STAGE(bufoff, gbase, voff) do { _Pragma("unroll") for (int _i = 0; _i < 2; ++_i) \
;         __builtin_amdgcn_global_load_lds((const unsigned*)((const char*)(gbase) + (voff)[_i]), (PG8_LAS unsigned*)(lds + (bufoff) + ldsw + _i * 8192), 16, 0, 0); } while (0)
; #define PG8_LDA(dst, b, h) do { _Pragma("unroll") for (int m = 0; m < 4; ++m) { const bf16x8 f0_ = *(const PG8_LAS bf16x8*)(lds + PG8_SA(b, h) + aoff + m * 2048), f1_ = *(const PG8_LAS bf16x8*)(lds + PG8_SA(b, h) + aoff + m * 2048 + 1024); dst[m].set(f0_, f1_); } } while (0)
; #define PG8_LDB(dst, b, h) do { _Pragma("unroll") for (int n = 0; n < 2; ++n) { const bf16x8 f0_ = *(const PG8_LAS bf16x8*)(lds + PG8_SB(b, h) + boff + n * 2048), f1_ = *(const PG8_LAS bf16x8*)(lds + PG8_SB(b, h) + boff + n * 2048 + 1024); dst[n].set(f0_, f1_); } } while (0)
; #define PG8_WAIT_V(n) asm volatile("s_waitcnt vmcnt(" #n ")" ::: "memory")
; #define PG8_WAIT_L(n) asm volatile("s_waitcnt lgkmcnt(" #n ")" ::: "memory")
; #define PG8_BAR __builtin_amdgcn_s_barrier()
; #define PG8_SCHED __builtin_amdgcn_sched_barrier(0)
; template <class Epi, class Sched, bool ALIGN_EPI = false, bool SP2 = false>
; __device__ __forceinline__ void gemm_phase(PG8_LAS unsigned char* lds, const Gemm g, const Sched& S, const Epi& E) {
;     ...
;             PG8_LDB(B0, 0, 0); PG8_LDB(B1, 0, 1); PG8_SCHED; PG8_LDA(At, 0, 0); PG8_STAGE(PG8_SA(1, 1), a1 + hstep, voffA);
;             PG8_WAIT_V(8); PG8_WAIT_L(0); PG8_BAR; PG8_MMA(0, 0, At, B0); PG8_MMA(0, 1, At, B1); PG8_BAR; PG8_SCHED;
;             PG8_LDA(At, 0, 1); PG8_STAGE(PG8_SB(0, 0), b2, voffB); PG8_STAGE(PG8_SB(0, 1), b2 + hstepB, voffB); PG8_STAGE(PG8_SA(0, 0), a2, voffA);
;             PG8_WAIT_V(8); PG8_WAIT_L(0); PG8_BAR; PG8_MMA(1, 0, At, B0); PG8_MMA(1, 1, At, B1); PG8_BAR; PG8_SCHED;
.Lkr2_a:
	v_lshl_add_u64 v[224:225], s[56:57], 0, v[176:177]
	s_add_i32 m0, s67, 0xc000
	ds_read_b128 v[162:165], v195
	ds_read_b128 v[186:189], v195 offset:1024
	ds_read_b128 v[198:201], v195 offset:2048
	ds_read_b128 v[202:205], v195 offset:3072
	ds_read_b128 v[206:209], v195 offset:4096
	ds_read_b128 v[212:215], v195 offset:5120
	ds_read_b128 v[216:219], v195 offset:6144
	ds_read_b128 v[220:223], v195 offset:7168
	global_load_lds_dwordx4 v[224:225], off
	v_lshl_add_u64 v[224:225], s[56:57], 0, v[178:179]
	s_add_i32 m0, s67, 0xe000
	s_nop 0
	global_load_lds_dwordx4 v[224:225], off
	s_waitcnt vmcnt(8)
	s_waitcnt lgkmcnt(0)
	s_barrier
	s_setprio 1
	s_waitcnt lgkmcnt(0)
	v_mfma_f32_16x16x32_bf16 v[126:129], v[130:133], v[162:165], v[126:129]
	v_mfma_f32_16x16x32_bf16 v[122:125], v[138:141], v[162:165], v[122:125]
	v_mfma_f32_16x16x32_bf16 v[58:61], v[130:133], v[198:201], v[58:61]
	v_mfma_f32_16x16x32_bf16 v[62:65], v[138:141], v[198:201], v[62:65]
	v_mfma_f32_16x16x32_bf16 v[106:109], v[130:133], v[206:209], v[106:109]
	v_mfma_f32_16x16x32_bf16 v[110:113], v[138:141], v[206:209], v[110:113]
	v_mfma_f32_16x16x32_bf16 v[98:101], v[130:133], v[216:219], v[98:101]
	v_mfma_f32_16x16x32_bf16 v[102:105], v[138:141], v[216:219], v[102:105]
	v_mfma_f32_16x16x32_bf16 v[126:129], v[134:137], v[186:189], v[126:129]
	v_mfma_f32_16x16x32_bf16 v[122:125], v[142:145], v[186:189], v[122:125]
	v_mfma_f32_16x16x32_bf16 v[58:61], v[134:137], v[202:205], v[58:61]
	v_mfma_f32_16x16x32_bf16 v[62:65], v[142:145], v[202:205], v[62:65]
	v_mfma_f32_16x16x32_bf16 v[106:109], v[134:137], v[212:215], v[106:109]
	v_mfma_f32_16x16x32_bf16 v[110:113], v[142:145], v[212:215], v[110:113]
	v_mfma_f32_16x16x32_bf16 v[98:101], v[134:137], v[220:223], v[98:101]
	v_mfma_f32_16x16x32_bf16 v[102:105], v[142:145], v[220:223], v[102:105]
	v_mfma_f32_16x16x32_bf16 v[118:121], v[146:149], v[162:165], v[118:121]
	v_mfma_f32_16x16x32_bf16 v[114:117], v[154:157], v[162:165], v[114:117]
	v_mfma_f32_16x16x32_bf16 v[50:53], v[146:149], v[198:201], v[50:53]
	v_mfma_f32_16x16x32_bf16 v[54:57], v[154:157], v[198:201], v[54:57]
	v_mfma_f32_16x16x32_bf16 v[90:93], v[146:149], v[206:209], v[90:93]
	v_mfma_f32_16x16x32_bf16 v[94:97], v[154:157], v[206:209], v[94:97]
	v_mfma_f32_16x16x32_bf16 v[74:77], v[146:149], v[216:219], v[74:77]
	v_mfma_f32_16x16x32_bf16 v[78:81], v[154:157], v[216:219], v[78:81]
	v_mfma_f32_16x16x32_bf16 v[118:121], v[150:153], v[186:189], v[118:121]
	v_mfma_f32_16x16x32_bf16 v[114:117], v[158:161], v[186:189], v[114:117]
	v_mfma_f32_16x16x32_bf16 v[50:53], v[150:153], v[202:205], v[50:53]
	v_mfma_f32_16x16x32_bf16 v[54:57], v[158:161], v[202:205], v[54:57]
	v_mfma_f32_16x16x32_bf16 v[90:93], v[150:153], v[212:215], v[90:93]
	v_mfma_f32_16x16x32_bf16 v[94:97], v[158:161], v[212:215], v[94:97]
	v_mfma_f32_16x16x32_bf16 v[74:77], v[150:153], v[220:223], v[74:77]
	v_mfma_f32_16x16x32_bf16 v[78:81], v[158:161], v[220:223], v[78:81]
	s_setprio 0
	s_barrier
	s_add_i32 s33, s82, s66
	v_lshl_add_u64 v[224:225], s[0:1], 0, v[168:169]
	s_mov_b32 m0, s33
	ds_read_b128 v[162:165], v195 offset:16384
	ds_read_b128 v[186:189], v195 offset:17408
	ds_read_b128 v[198:201], v195 offset:18432
	ds_read_b128 v[202:205], v195 offset:19456
	ds_read_b128 v[206:209], v195 offset:20480
	ds_read_b128 v[212:215], v195 offset:21504
	ds_read_b128 v[216:219], v195 offset:22528
	ds_read_b128 v[220:223], v195 offset:23552
	global_load_lds_dwordx4 v[224:225], off
	s_add_i32 m0, s33, 0x2000
	v_lshl_add_u64 v[226:227], s[0:1], 0, v[172:173]
	s_add_u32 s0, s0, s16
	s_addc_u32 s1, s1, s17
	s_add_i32 s33, s83, s66
	global_load_lds_dwordx4 v[226:227], off
	v_lshl_add_u64 v[228:229], s[0:1], 0, v[168:169]
	s_mov_b32 m0, s33
	v_lshl_add_u64 v[230:231], s[0:1], 0, v[172:173]
	global_load_lds_dwordx4 v[228:229], off
	s_add_i32 m0, s33, 0x2000
	v_lshl_add_u64 v[232:233], s[58:59], 0, v[166:167]
	global_load_lds_dwordx4 v[230:231], off
	v_lshl_add_u64 v[234:235], s[58:59], 0, v[170:171]
	s_waitcnt vmcnt(6)
	s_waitcnt lgkmcnt(0)
	s_barrier
	s_setprio 1
	s_waitcnt lgkmcnt(0)
	v_mfma_f32_16x16x32_bf16 v[82:85], v[130:133], v[162:165], v[82:85]
	v_mfma_f32_16x16x32_bf16 v[86:89], v[138:141], v[162:165], v[86:89]
	v_mfma_f32_16x16x32_bf16 v[46:49], v[130:133], v[198:201], v[46:49]
	v_mfma_f32_16x16x32_bf16 v[42:45], v[138:141], v[198:201], v[42:45]
	v_mfma_f32_16x16x32_bf16 v[30:33], v[130:133], v[206:209], v[30:33]
	v_mfma_f32_16x16x32_bf16 v[26:29], v[138:141], v[206:209], v[26:29]
	v_mfma_f32_16x16x32_bf16 v[14:17], v[130:133], v[216:219], v[14:17]
	v_mfma_f32_16x16x32_bf16 v[6:9], v[138:141], v[216:219], v[6:9]
	v_mfma_f32_16x16x32_bf16 v[82:85], v[134:137], v[186:189], v[82:85]
	v_mfma_f32_16x16x32_bf16 v[86:89], v[142:145], v[186:189], v[86:89]
	v_mfma_f32_16x16x32_bf16 v[46:49], v[134:137], v[202:205], v[46:49]
	v_mfma_f32_16x16x32_bf16 v[42:45], v[142:145], v[202:205], v[42:45]
	v_mfma_f32_16x16x32_bf16 v[30:33], v[134:137], v[212:215], v[30:33]
	v_mfma_f32_16x16x32_bf16 v[26:29], v[142:145], v[212:215], v[26:29]
	v_mfma_f32_16x16x32_bf16 v[14:17], v[134:137], v[220:223], v[14:17]
	v_mfma_f32_16x16x32_bf16 v[6:9], v[142:145], v[220:223], v[6:9]
	v_mfma_f32_16x16x32_bf16 v[66:69], v[146:149], v[162:165], v[66:69]
	v_mfma_f32_16x16x32_bf16 v[70:73], v[154:157], v[162:165], v[70:73]
	v_mfma_f32_16x16x32_bf16 v[38:41], v[146:149], v[198:201], v[38:41]
	v_mfma_f32_16x16x32_bf16 v[34:37], v[154:157], v[198:201], v[34:37]
	v_mfma_f32_16x16x32_bf16 v[22:25], v[146:149], v[206:209], v[22:25]
	v_mfma_f32_16x16x32_bf16 v[18:21], v[154:157], v[206:209], v[18:21]
	v_mfma_f32_16x16x32_bf16 v[10:13], v[146:149], v[216:219], v[10:13]
	v_mfma_f32_16x16x32_bf16 v[2:5], v[154:157], v[216:219], v[2:5]
	v_mfma_f32_16x16x32_bf16 v[66:69], v[150:153], v[186:189], v[66:69]
	v_mfma_f32_16x16x32_bf16 v[70:73], v[158:161], v[186:189], v[70:73]
	v_mfma_f32_16x16x32_bf16 v[38:41], v[150:153], v[202:205], v[38:41]
	v_mfma_f32_16x16x32_bf16 v[34:37], v[158:161], v[202:205], v[34:37]
	v_mfma_f32_16x16x32_bf16 v[22:25], v[150:153], v[212:215], v[22:25]
	v_mfma_f32_16x16x32_bf16 v[18:21], v[158:161], v[212:215], v[18:21]
	v_mfma_f32_16x16x32_bf16 v[10:13], v[150:153], v[220:223], v[10:13]
	v_mfma_f32_16x16x32_bf16 v[2:5], v[158:161], v[220:223], v[2:5]
	s_setprio 0
	s_barrier
; #define PG8_STAGE(bufoff, gbase, voff) do { _Pragma("unroll") for (int _i = 0; _i < 2; ++_i) \
;         __builtin_amdgcn_global_load_lds((const unsigned*)((const char*)(gbase) + (voff)[_i]), (PG8_LAS unsigned*)(lds + (bufoff) + ldsw + _i * 8192), 16, 0, 0); } while (0)
; #define PG8_LDA(dst, b, h) do { _Pragma("unroll") for (int m = 0; m < 4; ++m) { const bf16x8 f0_ = *(const PG8_LAS bf16x8*)(lds + PG8_SA(b, h) + aoff + m * 2048), f1_ = *(const PG8_LAS bf16x8*)(lds + PG8_SA(b, h) + aoff + m * 2048 + 1024); dst[m].set(f0_, f1_); } } while (0)
; #define PG8_LDB(dst, b, h) do { _Pragma("unroll") for (int n = 0; n < 2; ++n) { const bf16x8 f0_ = *(const PG8_LAS bf16x8*)(lds + PG8_SB(b, h) + boff + n * 2048), f1_ = *(const PG8_LAS bf16x8*)(lds + PG8_SB(b, h) + boff + n * 2048 + 1024); dst[n].set(f0_, f1_); } } while (0)
; #define PG8_WAIT_V(n) asm volatile("s_waitcnt vmcnt(" #n ")" ::: "memory")
; #define PG8_WAIT_L(n) asm volatile("s_waitcnt lgkmcnt(" #n ")" ::: "memory")
; #define PG8_BAR __builtin_amdgcn_s_barrier()
; #define PG8_SCHED __builtin_amdgcn_sched_barrier(0)
; template <class Epi, class Sched, bool ALIGN_EPI = false, bool SP2 = false>
; __device__ __forceinline__ void gemm_phase(PG8_LAS unsigned char* lds, const Gemm g, const Sched& S, const Epi& E) {
;     ...
;             PG8_LDB(B0, 1, 0); PG8_LDB(B1, 1, 1); PG8_SCHED; PG8_LDA(At, 1, 0); PG8_STAGE(PG8_SA(0, 1), a2 + hstep, voffA);
;             PG8_WAIT_V(8); PG8_WAIT_L(0); PG8_BAR; PG8_MMA(0, 0, At, B0); PG8_MMA(0, 1, At, B1); PG8_BAR; PG8_SCHED;
;             PG8_LDA(At, 1, 1); PG8_STAGE(PG8_SB(1, 0), b3, voffB); PG8_STAGE(PG8_SB(1, 1), b3 + hstepB, voffB); PG8_STAGE(PG8_SA(1, 0), a3, voffA);
	s_add_i32 s33, 0, 0x18000
	s_add_i32 s96, 0, 0x1c000
	v_add_u32_e32 v142, s33, v190
	v_add_u32_e32 v158, s96, v190
	ds_read_b128 v[130:133], v142
	ds_read_b128 v[134:137], v142 offset:1024
	ds_read_b128 v[138:141], v142 offset:2048
	ds_read_b128 v[142:145], v142 offset:3072
	ds_read_b128 v[146:149], v158
	ds_read_b128 v[150:153], v158 offset:1024
	ds_read_b128 v[154:157], v158 offset:2048
	ds_read_b128 v[158:161], v158 offset:3072
	s_add_u32 s0, s58, s14
	s_addc_u32 s1, s59, s15
	s_mov_b32 m0, s71
	v_lshl_add_u64 v[236:237], s[0:1], 0, v[166:167]
	ds_read_b128 v[162:165], v195 offset:32768
	ds_read_b128 v[186:189], v195 offset:33792
	ds_read_b128 v[198:201], v195 offset:34816
	ds_read_b128 v[202:205], v195 offset:35840
	ds_read_b128 v[206:209], v195 offset:36864
	ds_read_b128 v[212:215], v195 offset:37888
	ds_read_b128 v[216:219], v195 offset:38912
	ds_read_b128 v[220:223], v195 offset:39936
	s_mov_b32 m0, s67
	s_nop 0
	global_load_lds_dwordx4 v[232:233], off
	s_mov_b32 m0, s69
	s_nop 0
	global_load_lds_dwordx4 v[234:235], off
	s_mov_b32 m0, s71
	s_nop 0
	global_load_lds_dwordx4 v[236:237], off
	v_lshl_add_u64 v[236:237], s[0:1], 0, v[170:171]
	s_mov_b32 m0, s73
	s_nop 0
	global_load_lds_dwordx4 v[236:237], off
	s_waitcnt vmcnt(8)
	s_waitcnt lgkmcnt(0)
	s_barrier
	s_setprio 1
	s_waitcnt lgkmcnt(0)
	v_mfma_f32_16x16x32_bf16 v[126:129], v[130:133], v[162:165], v[126:129]
	v_mfma_f32_16x16x32_bf16 v[122:125], v[138:141], v[162:165], v[122:125]
	v_mfma_f32_16x16x32_bf16 v[58:61], v[130:133], v[198:201], v[58:61]
	v_mfma_f32_16x16x32_bf16 v[62:65], v[138:141], v[198:201], v[62:65]
	v_mfma_f32_16x16x32_bf16 v[106:109], v[130:133], v[206:209], v[106:109]
	v_mfma_f32_16x16x32_bf16 v[110:113], v[138:141], v[206:209], v[110:113]
	v_mfma_f32_16x16x32_bf16 v[98:101], v[130:133], v[216:219], v[98:101]
	v_mfma_f32_16x16x32_bf16 v[102:105], v[138:141], v[216:219], v[102:105]
	v_mfma_f32_16x16x32_bf16 v[126:129], v[134:137], v[186:189], v[126:129]
	v_mfma_f32_16x16x32_bf16 v[122:125], v[142:145], v[186:189], v[122:125]
	v_mfma_f32_16x16x32_bf16 v[58:61], v[134:137], v[202:205], v[58:61]
	v_mfma_f32_16x16x32_bf16 v[62:65], v[142:145], v[202:205], v[62:65]
	v_mfma_f32_16x16x32_bf16 v[106:109], v[134:137], v[212:215], v[106:109]
	v_mfma_f32_16x16x32_bf16 v[110:113], v[142:145], v[212:215], v[110:113]
	v_mfma_f32_16x16x32_bf16 v[98:101], v[134:137], v[220:223], v[98:101]
	v_mfma_f32_16x16x32_bf16 v[102:105], v[142:145], v[220:223], v[102:105]
	v_mfma_f32_16x16x32_bf16 v[118:121], v[146:149], v[162:165], v[118:121]
	v_mfma_f32_16x16x32_bf16 v[114:117], v[154:157], v[162:165], v[114:117]
	v_mfma_f32_16x16x32_bf16 v[50:53], v[146:149], v[198:201], v[50:53]
	v_mfma_f32_16x16x32_bf16 v[54:57], v[154:157], v[198:201], v[54:57]
	v_mfma_f32_16x16x32_bf16 v[90:93], v[146:149], v[206:209], v[90:93]
	v_mfma_f32_16x16x32_bf16 v[94:97], v[154:157], v[206:209], v[94:97]
	v_mfma_f32_16x16x32_bf16 v[74:77], v[146:149], v[216:219], v[74:77]
	v_mfma_f32_16x16x32_bf16 v[78:81], v[154:157], v[216:219], v[78:81]
	v_mfma_f32_16x16x32_bf16 v[118:121], v[150:153], v[186:189], v[118:121]
	v_mfma_f32_16x16x32_bf16 v[114:117], v[158:161], v[186:189], v[114:117]
	v_mfma_f32_16x16x32_bf16 v[50:53], v[150:153], v[202:205], v[50:53]
	v_mfma_f32_16x16x32_bf16 v[54:57], v[158:161], v[202:205], v[54:57]
	v_mfma_f32_16x16x32_bf16 v[90:93], v[150:153], v[212:215], v[90:93]
	v_mfma_f32_16x16x32_bf16 v[94:97], v[158:161], v[212:215], v[94:97]
	v_mfma_f32_16x16x32_bf16 v[74:77], v[150:153], v[220:223], v[74:77]
	v_mfma_f32_16x16x32_bf16 v[78:81], v[158:161], v[220:223], v[78:81]
	s_setprio 0
	s_barrier
	s_add_i32 s0, s33, s66
	s_add_i32 m0, s0, 0xffffff80
	ds_read_b128 v[162:165], v195 offset:49152
	ds_read_b128 v[186:189], v195 offset:50176
	ds_read_b128 v[198:201], v195 offset:51200
	ds_read_b128 v[202:205], v195 offset:52224
	ds_read_b128 v[206:209], v195 offset:53248
	ds_read_b128 v[212:215], v195 offset:54272
	ds_read_b128 v[216:219], v195 offset:55296
	ds_read_b128 v[220:223], v195 offset:56320
	global_load_lds_dwordx4 v[224:225], off offset:128
	s_add_i32 m0, s0, 0x1f80
	s_add_i32 s0, s96, s66
	global_load_lds_dwordx4 v[226:227], off offset:128
	s_add_i32 m0, s0, 0xffffff80
	s_nop 0
	global_load_lds_dwordx4 v[228:229], off offset:128
	s_add_i32 m0, s0, 0x1f80
	s_nop 0
	global_load_lds_dwordx4 v[230:231], off offset:128
	s_cmp_ge_i32 s95, s76
	s_cbranch_scc0 .Lkr2_b
	s_add_i32 m0, s74, 0xffffff80
	s_nop 0
	global_load_lds_dwordx4 v[232:233], off offset:128
	s_add_i32 m0, s75, 0xffffff80
	s_nop 0
	global_load_lds_dwordx4 v[234:235], off offset:128

; #define PG8_STAGE(bufoff, gbase, voff) do { _Pragma("unroll") for (int _i = 0; _i < 2; ++_i) \
;         __builtin_amdgcn_global_load_lds((const unsigned*)((const char*)(gbase) + (voff)[_i]), (PG8_LAS unsigned*)(lds + (bufoff) + ldsw + _i * 8192), 16, 0, 0); } while (0)
; #define PG8_LDA(dst, b, h) do { _Pragma("unroll") for (int m = 0; m < 4; ++m) { const bf16x8 f0_ = *(const PG8_LAS bf16x8*)(lds + PG8_SA(b, h) + aoff + m * 2048), f1_ = *(const PG8_LAS bf16x8*)(lds + PG8_SA(b, h) + aoff + m * 2048 + 1024); dst[m].set(f0_, f1_); } } while (0)
; #define PG8_LDB(dst, b, h) do { _Pragma("unroll") for (int n = 0; n < 2; ++n) { const bf16x8 f0_ = *(const PG8_LAS bf16x8*)(lds + PG8_SB(b, h) + boff + n * 2048), f1_ = *(const PG8_LAS bf16x8*)(lds + PG8_SB(b, h) + boff + n * 2048 + 1024); dst[n].set(f0_, f1_); } } while (0)
; #define PG8_WAIT_V(n) asm volatile("s_waitcnt vmcnt(" #n ")" ::: "memory")
; #define PG8_WAIT_L(n) asm volatile("s_waitcnt lgkmcnt(" #n ")" ::: "memory")
; #define PG8_BAR __builtin_amdgcn_s_barrier()
; #define PG8_SCHED __builtin_amdgcn_sched_barrier(0)
; template <class Epi, class Sched, bool ALIGN_EPI = false, bool SP2 = false>
; __device__ __forceinline__ void gemm_phase(PG8_LAS unsigned char* lds, const Gemm g, const Sched& S, const Epi& E) {
;     ...
;             PG8_LDB(B0, 0, 0); PG8_LDB(B1, 0, 1); PG8_SCHED; PG8_LDA(At, 0, 0); PG8_STAGE(PG8_SA(1, 1), a1 + hstep, voffA);
;             PG8_WAIT_V(8); PG8_WAIT_L(0); PG8_BAR; PG8_MMA(0, 0, At, B0); PG8_MMA(0, 1, At, B1); PG8_BAR; PG8_SCHED;
;             PG8_LDA(At, 0, 1); PG8_STAGE(PG8_SB(0, 0), b2, voffB); PG8_STAGE(PG8_SB(0, 1), b2 + hstepB, voffB); PG8_STAGE(PG8_SA(0, 0), a2, voffA);
;             PG8_WAIT_V(8); PG8_WAIT_L(0); PG8_BAR; PG8_MMA(1, 0, At, B0); PG8_MMA(1, 1, At, B1); PG8_BAR; PG8_SCHED;
.Lkr3_a:
	v_lshl_add_u64 v[148:149], s[30:31], 0, v[140:141]
	s_add_i32 m0, s40, 0xc000
	ds_read_b128 v[188:191], v154
	ds_read_b128 v[192:195], v154 offset:1024
	ds_read_b128 v[196:199], v154 offset:2048
	ds_read_b128 v[200:203], v154 offset:3072
	ds_read_b128 v[204:207], v154 offset:4096
	ds_read_b128 v[212:215], v154 offset:5120
	ds_read_b128 v[216:219], v154 offset:6144
	ds_read_b128 v[220:223], v154 offset:7168
	global_load_lds_dwordx4 v[148:149], off
	v_lshl_add_u64 v[148:149], s[30:31], 0, v[142:143]
	s_add_i32 m0, s40, 0xe000
	s_nop 0
	global_load_lds_dwordx4 v[148:149], off
	s_waitcnt vmcnt(8)
	s_waitcnt lgkmcnt(0)
	s_barrier
	s_setprio 1
	s_waitcnt lgkmcnt(0)
	v_mfma_f32_16x16x32_bf16 v[126:129], v[156:159], v[188:191], v[126:129]
	v_mfma_f32_16x16x32_bf16 v[122:125], v[164:167], v[188:191], v[122:125]
	v_mfma_f32_16x16x32_bf16 v[110:113], v[156:159], v[196:199], v[110:113]
	v_mfma_f32_16x16x32_bf16 v[106:109], v[164:167], v[196:199], v[106:109]
	v_mfma_f32_16x16x32_bf16 v[94:97], v[156:159], v[204:207], v[94:97]
	v_mfma_f32_16x16x32_bf16 v[90:93], v[164:167], v[204:207], v[90:93]
	v_mfma_f32_16x16x32_bf16 v[78:81], v[156:159], v[216:219], v[78:81]
	v_mfma_f32_16x16x32_bf16 v[74:77], v[164:167], v[216:219], v[74:77]
	v_mfma_f32_16x16x32_bf16 v[126:129], v[160:163], v[192:195], v[126:129]
	v_mfma_f32_16x16x32_bf16 v[122:125], v[168:171], v[192:195], v[122:125]
	v_mfma_f32_16x16x32_bf16 v[110:113], v[160:163], v[200:203], v[110:113]
	v_mfma_f32_16x16x32_bf16 v[106:109], v[168:171], v[200:203], v[106:109]
	v_mfma_f32_16x16x32_bf16 v[94:97], v[160:163], v[212:215], v[94:97]
	v_mfma_f32_16x16x32_bf16 v[90:93], v[168:171], v[212:215], v[90:93]
	v_mfma_f32_16x16x32_bf16 v[78:81], v[160:163], v[220:223], v[78:81]
	v_mfma_f32_16x16x32_bf16 v[74:77], v[168:171], v[220:223], v[74:77]
	v_mfma_f32_16x16x32_bf16 v[118:121], v[172:175], v[188:191], v[118:121]
	v_mfma_f32_16x16x32_bf16 v[114:117], v[180:183], v[188:191], v[114:117]
	v_mfma_f32_16x16x32_bf16 v[102:105], v[172:175], v[196:199], v[102:105]
	v_mfma_f32_16x16x32_bf16 v[98:101], v[180:183], v[196:199], v[98:101]
	v_mfma_f32_16x16x32_bf16 v[86:89], v[172:175], v[204:207], v[86:89]
	v_mfma_f32_16x16x32_bf16 v[82:85], v[180:183], v[204:207], v[82:85]
	v_mfma_f32_16x16x32_bf16 v[70:73], v[172:175], v[216:219], v[70:73]
	v_mfma_f32_16x16x32_bf16 v[66:69], v[180:183], v[216:219], v[66:69]
	v_mfma_f32_16x16x32_bf16 v[118:121], v[176:179], v[192:195], v[118:121]
	v_mfma_f32_16x16x32_bf16 v[114:117], v[184:187], v[192:195], v[114:117]
	v_mfma_f32_16x16x32_bf16 v[102:105], v[176:179], v[200:203], v[102:105]
	v_mfma_f32_16x16x32_bf16 v[98:101], v[184:187], v[200:203], v[98:101]
	v_mfma_f32_16x16x32_bf16 v[86:89], v[176:179], v[212:215], v[86:89]
	v_mfma_f32_16x16x32_bf16 v[82:85], v[184:187], v[212:215], v[82:85]
	v_mfma_f32_16x16x32_bf16 v[70:73], v[176:179], v[220:223], v[70:73]
	v_mfma_f32_16x16x32_bf16 v[66:69], v[184:187], v[220:223], v[66:69]
	s_setprio 0
	s_barrier
	s_add_i32 s33, s52, s39
	v_lshl_add_u64 v[148:149], s[0:1], 0, v[132:133]
	s_mov_b32 m0, s33
	ds_read_b128 v[188:191], v154 offset:16384
	ds_read_b128 v[192:195], v154 offset:17408
	ds_read_b128 v[196:199], v154 offset:18432
	ds_read_b128 v[200:203], v154 offset:19456
	ds_read_b128 v[204:207], v154 offset:20480
	ds_read_b128 v[212:215], v154 offset:21504
	ds_read_b128 v[216:219], v154 offset:22528
	ds_read_b128 v[220:223], v154 offset:23552
	global_load_lds_dwordx4 v[148:149], off
	s_add_i32 m0, s33, 0x2000
	v_lshl_add_u64 v[208:209], s[0:1], 0, v[136:137]
	s_add_u32 s0, s0, s14
	s_addc_u32 s1, s1, s15
	s_add_i32 s33, s53, s39
	global_load_lds_dwordx4 v[208:209], off
	v_lshl_add_u64 v[224:225], s[0:1], 0, v[132:133]
	s_mov_b32 m0, s33
	v_lshl_add_u64 v[226:227], s[0:1], 0, v[136:137]
	global_load_lds_dwordx4 v[224:225], off
	s_add_i32 m0, s33, 0x2000
	v_lshl_add_u64 v[228:229], s[34:35], 0, v[130:131]
	global_load_lds_dwordx4 v[226:227], off
	v_lshl_add_u64 v[230:231], s[34:35], 0, v[134:135]
	s_waitcnt vmcnt(6)
	s_waitcnt lgkmcnt(0)
	s_barrier
	s_setprio 1
	s_waitcnt lgkmcnt(0)
	v_mfma_f32_16x16x32_bf16 v[62:65], v[156:159], v[188:191], v[62:65]
	v_mfma_f32_16x16x32_bf16 v[58:61], v[164:167], v[188:191], v[58:61]
	v_mfma_f32_16x16x32_bf16 v[46:49], v[156:159], v[196:199], v[46:49]
	v_mfma_f32_16x16x32_bf16 v[42:45], v[164:167], v[196:199], v[42:45]
	v_mfma_f32_16x16x32_bf16 v[30:33], v[156:159], v[204:207], v[30:33]
	v_mfma_f32_16x16x32_bf16 v[26:29], v[164:167], v[204:207], v[26:29]
	v_mfma_f32_16x16x32_bf16 v[14:17], v[156:159], v[216:219], v[14:17]
	v_mfma_f32_16x16x32_bf16 v[6:9], v[164:167], v[216:219], v[6:9]
	v_mfma_f32_16x16x32_bf16 v[62:65], v[160:163], v[192:195], v[62:65]
	v_mfma_f32_16x16x32_bf16 v[58:61], v[168:171], v[192:195], v[58:61]
	v_mfma_f32_16x16x32_bf16 v[46:49], v[160:163], v[200:203], v[46:49]
	v_mfma_f32_16x16x32_bf16 v[42:45], v[168:171], v[200:203], v[42:45]
	v_mfma_f32_16x16x32_bf16 v[30:33], v[160:163], v[212:215], v[30:33]
	v_mfma_f32_16x16x32_bf16 v[26:29], v[168:171], v[212:215], v[26:29]
	v_mfma_f32_16x16x32_bf16 v[14:17], v[160:163], v[220:223], v[14:17]
	v_mfma_f32_16x16x32_bf16 v[6:9], v[168:171], v[220:223], v[6:9]
	v_mfma_f32_16x16x32_bf16 v[54:57], v[172:175], v[188:191], v[54:57]
	v_mfma_f32_16x16x32_bf16 v[50:53], v[180:183], v[188:191], v[50:53]
	v_mfma_f32_16x16x32_bf16 v[38:41], v[172:175], v[196:199], v[38:41]
	v_mfma_f32_16x16x32_bf16 v[34:37], v[180:183], v[196:199], v[34:37]
	v_mfma_f32_16x16x32_bf16 v[22:25], v[172:175], v[204:207], v[22:25]
	v_mfma_f32_16x16x32_bf16 v[18:21], v[180:183], v[204:207], v[18:21]
	v_mfma_f32_16x16x32_bf16 v[10:13], v[172:175], v[216:219], v[10:13]
	v_mfma_f32_16x16x32_bf16 v[2:5], v[180:183], v[216:219], v[2:5]
	v_mfma_f32_16x16x32_bf16 v[54:57], v[176:179], v[192:195], v[54:57]
	v_mfma_f32_16x16x32_bf16 v[50:53], v[184:187], v[192:195], v[50:53]
	v_mfma_f32_16x16x32_bf16 v[38:41], v[176:179], v[200:203], v[38:41]
	v_mfma_f32_16x16x32_bf16 v[34:37], v[184:187], v[200:203], v[34:37]
	v_mfma_f32_16x16x32_bf16 v[22:25], v[176:179], v[212:215], v[22:25]
	v_mfma_f32_16x16x32_bf16 v[18:21], v[184:187], v[212:215], v[18:21]
	v_mfma_f32_16x16x32_bf16 v[10:13], v[176:179], v[220:223], v[10:13]
	v_mfma_f32_16x16x32_bf16 v[2:5], v[184:187], v[220:223], v[2:5]
	s_setprio 0
	s_barrier
; #define PG8_STAGE(bufoff, gbase, voff) do { _Pragma("unroll") for (int _i = 0; _i < 2; ++_i) \
;         __builtin_amdgcn_global_load_lds((const unsigned*)((const char*)(gbase) + (voff)[_i]), (PG8_LAS unsigned*)(lds + (bufoff) + ldsw + _i * 8192), 16, 0, 0); } while (0)
; #define PG8_LDA(dst, b, h) do { _Pragma("unroll") for (int m = 0; m < 4; ++m) { const bf16x8 f0_ = *(const PG8_LAS bf16x8*)(lds + PG8_SA(b, h) + aoff + m * 2048), f1_ = *(const PG8_LAS bf16x8*)(lds + PG8_SA(b, h) + aoff + m * 2048 + 1024); dst[m].set(f0_, f1_); } } while (0)
; #define PG8_LDB(dst, b, h) do { _Pragma("unroll") for (int n = 0; n < 2; ++n) { const bf16x8 f0_ = *(const PG8_LAS bf16x8*)(lds + PG8_SB(b, h) + boff + n * 2048), f1_ = *(const PG8_LAS bf16x8*)(lds + PG8_SB(b, h) + boff + n * 2048 + 1024); dst[n].set(f0_, f1_); } } while (0)
; #define PG8_WAIT_V(n) asm volatile("s_waitcnt vmcnt(" #n ")" ::: "memory")
; #define PG8_WAIT_L(n) asm volatile("s_waitcnt lgkmcnt(" #n ")" ::: "memory")
; #define PG8_BAR __builtin_amdgcn_s_barrier()
; #define PG8_SCHED __builtin_amdgcn_sched_barrier(0)
; template <class Epi, class Sched, bool ALIGN_EPI = false, bool SP2 = false>
; __device__ __forceinline__ void gemm_phase(PG8_LAS unsigned char* lds, const Gemm g, const Sched& S, const Epi& E) {
;     ...
;             PG8_LDB(B0, 1, 0); PG8_LDB(B1, 1, 1); PG8_SCHED; PG8_LDA(At, 1, 0); PG8_STAGE(PG8_SA(0, 1), a2 + hstep, voffA);
;             PG8_WAIT_V(8); PG8_WAIT_L(0); PG8_BAR; PG8_MMA(0, 0, At, B0); PG8_MMA(0, 1, At, B1); PG8_BAR; PG8_SCHED;
;             PG8_LDA(At, 1, 1); PG8_STAGE(PG8_SB(1, 0), b3, voffB); PG8_STAGE(PG8_SB(1, 1), b3 + hstepB, voffB); PG8_STAGE(PG8_SA(1, 0), a3, voffA);
	s_add_i32 s33, 0, 0x18000
	s_add_i32 s63, 0, 0x1c000
	v_add_u32_e32 v168, s33, v1
	v_add_u32_e32 v184, s63, v1
	ds_read_b128 v[156:159], v168
	ds_read_b128 v[160:163], v168 offset:1024
	ds_read_b128 v[164:167], v168 offset:2048
	ds_read_b128 v[168:171], v168 offset:3072
	ds_read_b128 v[172:175], v184
	ds_read_b128 v[176:179], v184 offset:1024
	ds_read_b128 v[180:183], v184 offset:2048
	ds_read_b128 v[184:187], v184 offset:3072
	s_add_u32 s0, s34, s12
	s_addc_u32 s1, s35, s13
	s_mov_b32 m0, s42
	v_lshl_add_u64 v[232:233], s[0:1], 0, v[130:131]
	ds_read_b128 v[188:191], v154 offset:32768
	ds_read_b128 v[192:195], v154 offset:33792
	ds_read_b128 v[196:199], v154 offset:34816
	ds_read_b128 v[200:203], v154 offset:35840
	ds_read_b128 v[204:207], v154 offset:36864
	ds_read_b128 v[212:215], v154 offset:37888
	ds_read_b128 v[216:219], v154 offset:38912
	ds_read_b128 v[220:223], v154 offset:39936
	s_mov_b32 m0, s40
	s_nop 0
	global_load_lds_dwordx4 v[228:229], off
	s_mov_b32 m0, s41
	s_nop 0
	global_load_lds_dwordx4 v[230:231], off
	s_mov_b32 m0, s42
	s_nop 0
	global_load_lds_dwordx4 v[232:233], off
	v_lshl_add_u64 v[232:233], s[0:1], 0, v[134:135]
	s_mov_b32 m0, s43
	s_nop 0
	global_load_lds_dwordx4 v[232:233], off
	s_waitcnt vmcnt(8)
	s_waitcnt lgkmcnt(0)
	s_barrier
	s_setprio 1
	s_waitcnt lgkmcnt(0)
	v_mfma_f32_16x16x32_bf16 v[126:129], v[156:159], v[188:191], v[126:129]
	v_mfma_f32_16x16x32_bf16 v[122:125], v[164:167], v[188:191], v[122:125]
	v_mfma_f32_16x16x32_bf16 v[110:113], v[156:159], v[196:199], v[110:113]
	v_mfma_f32_16x16x32_bf16 v[106:109], v[164:167], v[196:199], v[106:109]
	v_mfma_f32_16x16x32_bf16 v[94:97], v[156:159], v[204:207], v[94:97]
	v_mfma_f32_16x16x32_bf16 v[90:93], v[164:167], v[204:207], v[90:93]
	v_mfma_f32_16x16x32_bf16 v[78:81], v[156:159], v[216:219], v[78:81]
	v_mfma_f32_16x16x32_bf16 v[74:77], v[164:167], v[216:219], v[74:77]
	v_mfma_f32_16x16x32_bf16 v[126:129], v[160:163], v[192:195], v[126:129]
	v_mfma_f32_16x16x32_bf16 v[122:125], v[168:171], v[192:195], v[122:125]
	v_mfma_f32_16x16x32_bf16 v[110:113], v[160:163], v[200:203], v[110:113]
	v_mfma_f32_16x16x32_bf16 v[106:109], v[168:171], v[200:203], v[106:109]
	v_mfma_f32_16x16x32_bf16 v[94:97], v[160:163], v[212:215], v[94:97]
	v_mfma_f32_16x16x32_bf16 v[90:93], v[168:171], v[212:215], v[90:93]
	v_mfma_f32_16x16x32_bf16 v[78:81], v[160:163], v[220:223], v[78:81]
	v_mfma_f32_16x16x32_bf16 v[74:77], v[168:171], v[220:223], v[74:77]
	v_mfma_f32_16x16x32_bf16 v[118:121], v[172:175], v[188:191], v[118:121]
	v_mfma_f32_16x16x32_bf16 v[114:117], v[180:183], v[188:191], v[114:117]
	v_mfma_f32_16x16x32_bf16 v[102:105], v[172:175], v[196:199], v[102:105]
	v_mfma_f32_16x16x32_bf16 v[98:101], v[180:183], v[196:199], v[98:101]
	v_mfma_f32_16x16x32_bf16 v[86:89], v[172:175], v[204:207], v[86:89]
	v_mfma_f32_16x16x32_bf16 v[82:85], v[180:183], v[204:207], v[82:85]
	v_mfma_f32_16x16x32_bf16 v[70:73], v[172:175], v[216:219], v[70:73]
	v_mfma_f32_16x16x32_bf16 v[66:69], v[180:183], v[216:219], v[66:69]
	v_mfma_f32_16x16x32_bf16 v[118:121], v[176:179], v[192:195], v[118:121]
	v_mfma_f32_16x16x32_bf16 v[114:117], v[184:187], v[192:195], v[114:117]
	v_mfma_f32_16x16x32_bf16 v[102:105], v[176:179], v[200:203], v[102:105]
	v_mfma_f32_16x16x32_bf16 v[98:101], v[184:187], v[200:203], v[98:101]
	v_mfma_f32_16x16x32_bf16 v[86:89], v[176:179], v[212:215], v[86:89]
	v_mfma_f32_16x16x32_bf16 v[82:85], v[184:187], v[212:215], v[82:85]
	v_mfma_f32_16x16x32_bf16 v[70:73], v[176:179], v[220:223], v[70:73]
	v_mfma_f32_16x16x32_bf16 v[66:69], v[184:187], v[220:223], v[66:69]
	s_setprio 0
	s_barrier
	s_add_i32 s0, s33, s39
	s_add_i32 m0, s0, 0xffffff80
	ds_read_b128 v[188:191], v154 offset:49152
	ds_read_b128 v[192:195], v154 offset:50176
	ds_read_b128 v[196:199], v154 offset:51200
	ds_read_b128 v[200:203], v154 offset:52224
	ds_read_b128 v[204:207], v154 offset:53248
	ds_read_b128 v[212:215], v154 offset:54272
	ds_read_b128 v[216:219], v154 offset:55296
	ds_read_b128 v[220:223], v154 offset:56320
	global_load_lds_dwordx4 v[148:149], off offset:128
	s_add_i32 m0, s0, 0x1f80
	s_add_i32 s0, s63, s39
	global_load_lds_dwordx4 v[208:209], off offset:128
	s_add_i32 m0, s0, 0xffffff80
	s_nop 0
	global_load_lds_dwordx4 v[224:225], off offset:128
	s_add_i32 m0, s0, 0x1f80
	s_nop 0
	global_load_lds_dwordx4 v[226:227], off offset:128
	s_cmp_ge_i32 s61, s47
	s_cbranch_scc0 .Lkr3_b
	s_add_i32 m0, s45, 0xffffff80
	s_nop 0
	global_load_lds_dwordx4 v[228:229], off offset:128
	s_add_i32 m0, s46, 0xffffff80
	s_nop 0
	global_load_lds_dwordx4 v[230:231], off offset:128

; #define PG8_STAGE(bufoff, gbase, voff) do { _Pragma("unroll") for (int _i = 0; _i < 2; ++_i) \
;         __builtin_amdgcn_global_load_lds((const unsigned*)((const char*)(gbase) + (voff)[_i]), (PG8_LAS unsigned*)(lds + (bufoff) + ldsw + _i * 8192), 16, 0, 0); } while (0)
; #define PG8_LDA(dst, b, h) do { _Pragma("unroll") for (int m = 0; m < 4; ++m) { const bf16x8 f0_ = *(const PG8_LAS bf16x8*)(lds + PG8_SA(b, h) + aoff + m * 2048), f1_ = *(const PG8_LAS bf16x8*)(lds + PG8_SA(b, h) + aoff + m * 2048 + 1024); dst[m].set(f0_, f1_); } } while (0)
; #define PG8_LDB(dst, b, h) do { _Pragma("unroll") for (int n = 0; n < 2; ++n) { const bf16x8 f0_ = *(const PG8_LAS bf16x8*)(lds + PG8_SB(b, h) + boff + n * 2048), f1_ = *(const PG8_LAS bf16x8*)(lds + PG8_SB(b, h) + boff + n * 2048 + 1024); dst[n].set(f0_, f1_); } } while (0)
; #define PG8_WAIT_V(n) asm volatile("s_waitcnt vmcnt(" #n ")" ::: "memory")
; #define PG8_WAIT_L(n) asm volatile("s_waitcnt lgkmcnt(" #n ")" ::: "memory")
; #define PG8_BAR __builtin_amdgcn_s_barrier()
; #define PG8_SCHED __builtin_amdgcn_sched_barrier(0)
; template <class Epi, class Sched, bool ALIGN_EPI = false, bool SP2 = false>
; __device__ __forceinline__ void gemm_phase(PG8_LAS unsigned char* lds, const Gemm g, const Sched& S, const Epi& E) {
;     ...
;             PG8_LDB(B0, 0, 0); PG8_LDB(B1, 0, 1); PG8_SCHED; PG8_LDA(At, 0, 0); PG8_STAGE(PG8_SA(1, 1), a1 + hstep, voffA);
;             PG8_WAIT_V(8); PG8_WAIT_L(0); PG8_BAR; PG8_MMA(0, 0, At, B0); PG8_MMA(0, 1, At, B1); PG8_BAR; PG8_SCHED;
;             PG8_LDA(At, 0, 1); PG8_STAGE(PG8_SB(0, 0), b2, voffB); PG8_STAGE(PG8_SB(0, 1), b2 + hstepB, voffB); PG8_STAGE(PG8_SA(0, 0), a2, voffA);
;             PG8_WAIT_V(8); PG8_WAIT_L(0); PG8_BAR; PG8_MMA(1, 0, At, B0); PG8_MMA(1, 1, At, B1); PG8_BAR; PG8_SCHED;
.Lkr4_a:
	v_lshl_add_u64 v[148:149], s[30:31], 0, v[140:141]
	s_add_i32 m0, s40, 0xc000
	ds_read_b128 v[188:191], v154
	ds_read_b128 v[192:195], v154 offset:1024
	ds_read_b128 v[196:199], v154 offset:2048
	ds_read_b128 v[200:203], v154 offset:3072
	ds_read_b128 v[204:207], v154 offset:4096
	ds_read_b128 v[212:215], v154 offset:5120
	ds_read_b128 v[216:219], v154 offset:6144
	ds_read_b128 v[220:223], v154 offset:7168
	global_load_lds_dwordx4 v[148:149], off
	v_lshl_add_u64 v[148:149], s[30:31], 0, v[142:143]
	s_add_i32 m0, s40, 0xe000
	s_nop 0
	global_load_lds_dwordx4 v[148:149], off
	s_waitcnt vmcnt(8)
	s_waitcnt lgkmcnt(0)
	s_barrier
	s_setprio 1
	s_waitcnt lgkmcnt(0)
	v_mfma_f32_16x16x32_bf16 v[126:129], v[156:159], v[188:191], v[126:129]
	v_mfma_f32_16x16x32_bf16 v[122:125], v[164:167], v[188:191], v[122:125]
	v_mfma_f32_16x16x32_bf16 v[110:113], v[156:159], v[196:199], v[110:113]
	v_mfma_f32_16x16x32_bf16 v[106:109], v[164:167], v[196:199], v[106:109]
	v_mfma_f32_16x16x32_bf16 v[94:97], v[156:159], v[204:207], v[94:97]
	v_mfma_f32_16x16x32_bf16 v[90:93], v[164:167], v[204:207], v[90:93]
	v_mfma_f32_16x16x32_bf16 v[78:81], v[156:159], v[216:219], v[78:81]
	v_mfma_f32_16x16x32_bf16 v[74:77], v[164:167], v[216:219], v[74:77]
	v_mfma_f32_16x16x32_bf16 v[126:129], v[160:163], v[192:195], v[126:129]
	v_mfma_f32_16x16x32_bf16 v[122:125], v[168:171], v[192:195], v[122:125]
	v_mfma_f32_16x16x32_bf16 v[110:113], v[160:163], v[200:203], v[110:113]
	v_mfma_f32_16x16x32_bf16 v[106:109], v[168:171], v[200:203], v[106:109]
	v_mfma_f32_16x16x32_bf16 v[94:97], v[160:163], v[212:215], v[94:97]
	v_mfma_f32_16x16x32_bf16 v[90:93], v[168:171], v[212:215], v[90:93]
	v_mfma_f32_16x16x32_bf16 v[78:81], v[160:163], v[220:223], v[78:81]
	v_mfma_f32_16x16x32_bf16 v[74:77], v[168:171], v[220:223], v[74:77]
	v_mfma_f32_16x16x32_bf16 v[118:121], v[172:175], v[188:191], v[118:121]
	v_mfma_f32_16x16x32_bf16 v[114:117], v[180:183], v[188:191], v[114:117]
	v_mfma_f32_16x16x32_bf16 v[102:105], v[172:175], v[196:199], v[102:105]
	v_mfma_f32_16x16x32_bf16 v[98:101], v[180:183], v[196:199], v[98:101]
	v_mfma_f32_16x16x32_bf16 v[86:89], v[172:175], v[204:207], v[86:89]
	v_mfma_f32_16x16x32_bf16 v[82:85], v[180:183], v[204:207], v[82:85]
	v_mfma_f32_16x16x32_bf16 v[70:73], v[172:175], v[216:219], v[70:73]
	v_mfma_f32_16x16x32_bf16 v[66:69], v[180:183], v[216:219], v[66:69]
	v_mfma_f32_16x16x32_bf16 v[118:121], v[176:179], v[192:195], v[118:121]
	v_mfma_f32_16x16x32_bf16 v[114:117], v[184:187], v[192:195], v[114:117]
	v_mfma_f32_16x16x32_bf16 v[102:105], v[176:179], v[200:203], v[102:105]
	v_mfma_f32_16x16x32_bf16 v[98:101], v[184:187], v[200:203], v[98:101]
	v_mfma_f32_16x16x32_bf16 v[86:89], v[176:179], v[212:215], v[86:89]
	v_mfma_f32_16x16x32_bf16 v[82:85], v[184:187], v[212:215], v[82:85]
	v_mfma_f32_16x16x32_bf16 v[70:73], v[176:179], v[220:223], v[70:73]
	v_mfma_f32_16x16x32_bf16 v[66:69], v[184:187], v[220:223], v[66:69]
	s_setprio 0
	s_barrier
	s_add_i32 s33, s52, s39
	v_lshl_add_u64 v[148:149], s[0:1], 0, v[132:133]
	s_mov_b32 m0, s33
	ds_read_b128 v[188:191], v154 offset:16384
	ds_read_b128 v[192:195], v154 offset:17408
	ds_read_b128 v[196:199], v154 offset:18432
	ds_read_b128 v[200:203], v154 offset:19456
	ds_read_b128 v[204:207], v154 offset:20480
	ds_read_b128 v[212:215], v154 offset:21504
	ds_read_b128 v[216:219], v154 offset:22528
	ds_read_b128 v[220:223], v154 offset:23552
	global_load_lds_dwordx4 v[148:149], off
	s_add_i32 m0, s33, 0x2000
	v_lshl_add_u64 v[208:209], s[0:1], 0, v[136:137]
	s_add_u32 s0, s0, s14
	s_addc_u32 s1, s1, s15
	s_add_i32 s33, s53, s39
	global_load_lds_dwordx4 v[208:209], off
	v_lshl_add_u64 v[224:225], s[0:1], 0, v[132:133]
	s_mov_b32 m0, s33
	v_lshl_add_u64 v[226:227], s[0:1], 0, v[136:137]
	global_load_lds_dwordx4 v[224:225], off
	s_add_i32 m0, s33, 0x2000
	v_lshl_add_u64 v[228:229], s[34:35], 0, v[130:131]
	global_load_lds_dwordx4 v[226:227], off
	v_lshl_add_u64 v[230:231], s[34:35], 0, v[134:135]
	s_waitcnt vmcnt(6)
	s_waitcnt lgkmcnt(0)
	s_barrier
	s_setprio 1
	s_waitcnt lgkmcnt(0)
	v_mfma_f32_16x16x32_bf16 v[62:65], v[156:159], v[188:191], v[62:65]
	v_mfma_f32_16x16x32_bf16 v[58:61], v[164:167], v[188:191], v[58:61]
	v_mfma_f32_16x16x32_bf16 v[46:49], v[156:159], v[196:199], v[46:49]
	v_mfma_f32_16x16x32_bf16 v[42:45], v[164:167], v[196:199], v[42:45]
	v_mfma_f32_16x16x32_bf16 v[30:33], v[156:159], v[204:207], v[30:33]
	v_mfma_f32_16x16x32_bf16 v[26:29], v[164:167], v[204:207], v[26:29]
	v_mfma_f32_16x16x32_bf16 v[14:17], v[156:159], v[216:219], v[14:17]
	v_mfma_f32_16x16x32_bf16 v[6:9], v[164:167], v[216:219], v[6:9]
	v_mfma_f32_16x16x32_bf16 v[62:65], v[160:163], v[192:195], v[62:65]
	v_mfma_f32_16x16x32_bf16 v[58:61], v[168:171], v[192:195], v[58:61]
	v_mfma_f32_16x16x32_bf16 v[46:49], v[160:163], v[200:203], v[46:49]
	v_mfma_f32_16x16x32_bf16 v[42:45], v[168:171], v[200:203], v[42:45]
	v_mfma_f32_16x16x32_bf16 v[30:33], v[160:163], v[212:215], v[30:33]
	v_mfma_f32_16x16x32_bf16 v[26:29], v[168:171], v[212:215], v[26:29]
	v_mfma_f32_16x16x32_bf16 v[14:17], v[160:163], v[220:223], v[14:17]
	v_mfma_f32_16x16x32_bf16 v[6:9], v[168:171], v[220:223], v[6:9]
	v_mfma_f32_16x16x32_bf16 v[54:57], v[172:175], v[188:191], v[54:57]
	v_mfma_f32_16x16x32_bf16 v[50:53], v[180:183], v[188:191], v[50:53]
	v_mfma_f32_16x16x32_bf16 v[38:41], v[172:175], v[196:199], v[38:41]
	v_mfma_f32_16x16x32_bf16 v[34:37], v[180:183], v[196:199], v[34:37]
	v_mfma_f32_16x16x32_bf16 v[22:25], v[172:175], v[204:207], v[22:25]
	v_mfma_f32_16x16x32_bf16 v[18:21], v[180:183], v[204:207], v[18:21]
	v_mfma_f32_16x16x32_bf16 v[10:13], v[172:175], v[216:219], v[10:13]
	v_mfma_f32_16x16x32_bf16 v[2:5], v[180:183], v[216:219], v[2:5]
	v_mfma_f32_16x16x32_bf16 v[54:57], v[176:179], v[192:195], v[54:57]
	v_mfma_f32_16x16x32_bf16 v[50:53], v[184:187], v[192:195], v[50:53]
	v_mfma_f32_16x16x32_bf16 v[38:41], v[176:179], v[200:203], v[38:41]
	v_mfma_f32_16x16x32_bf16 v[34:37], v[184:187], v[200:203], v[34:37]
	v_mfma_f32_16x16x32_bf16 v[22:25], v[176:179], v[212:215], v[22:25]
	v_mfma_f32_16x16x32_bf16 v[18:21], v[184:187], v[212:215], v[18:21]
	v_mfma_f32_16x16x32_bf16 v[10:13], v[176:179], v[220:223], v[10:13]
	v_mfma_f32_16x16x32_bf16 v[2:5], v[184:187], v[220:223], v[2:5]
	s_setprio 0
	s_barrier
; #define PG8_STAGE(bufoff, gbase, voff) do { _Pragma("unroll") for (int _i = 0; _i < 2; ++_i) \
;         __builtin_amdgcn_global_load_lds((const unsigned*)((const char*)(gbase) + (voff)[_i]), (PG8_LAS unsigned*)(lds + (bufoff) + ldsw + _i * 8192), 16, 0, 0); } while (0)
; #define PG8_LDA(dst, b, h) do { _Pragma("unroll") for (int m = 0; m < 4; ++m) { const bf16x8 f0_ = *(const PG8_LAS bf16x8*)(lds + PG8_SA(b, h) + aoff + m * 2048), f1_ = *(const PG8_LAS bf16x8*)(lds + PG8_SA(b, h) + aoff + m * 2048 + 1024); dst[m].set(f0_, f1_); } } while (0)
; #define PG8_LDB(dst, b, h) do { _Pragma("unroll") for (int n = 0; n < 2; ++n) { const bf16x8 f0_ = *(const PG8_LAS bf16x8*)(lds + PG8_SB(b, h) + boff + n * 2048), f1_ = *(const PG8_LAS bf16x8*)(lds + PG8_SB(b, h) + boff + n * 2048 + 1024); dst[n].set(f0_, f1_); } } while (0)
; #define PG8_WAIT_V(n) asm volatile("s_waitcnt vmcnt(" #n ")" ::: "memory")
; #define PG8_WAIT_L(n) asm volatile("s_waitcnt lgkmcnt(" #n ")" ::: "memory")
; #define PG8_BAR __builtin_amdgcn_s_barrier()
; #define PG8_SCHED __builtin_amdgcn_sched_barrier(0)
; template <class Epi, class Sched, bool ALIGN_EPI = false, bool SP2 = false>
; __device__ __forceinline__ void gemm_phase(PG8_LAS unsigned char* lds, const Gemm g, const Sched& S, const Epi& E) {
;     ...
;             PG8_LDB(B0, 1, 0); PG8_LDB(B1, 1, 1); PG8_SCHED; PG8_LDA(At, 1, 0); PG8_STAGE(PG8_SA(0, 1), a2 + hstep, voffA);
;             PG8_WAIT_V(8); PG8_WAIT_L(0); PG8_BAR; PG8_MMA(0, 0, At, B0); PG8_MMA(0, 1, At, B1); PG8_BAR; PG8_SCHED;
;             PG8_LDA(At, 1, 1); PG8_STAGE(PG8_SB(1, 0), b3, voffB); PG8_STAGE(PG8_SB(1, 1), b3 + hstepB, voffB); PG8_STAGE(PG8_SA(1, 0), a3, voffA);
	s_add_i32 s33, 0, 0x18000
	s_add_i32 s63, 0, 0x1c000
	v_add_u32_e32 v168, s33, v1
	v_add_u32_e32 v184, s63, v1
	ds_read_b128 v[156:159], v168
	ds_read_b128 v[160:163], v168 offset:1024
	ds_read_b128 v[164:167], v168 offset:2048
	ds_read_b128 v[168:171], v168 offset:3072
	ds_read_b128 v[172:175], v184
	ds_read_b128 v[176:179], v184 offset:1024
	ds_read_b128 v[180:183], v184 offset:2048
	ds_read_b128 v[184:187], v184 offset:3072
	s_add_u32 s0, s34, s12
	s_addc_u32 s1, s35, s13
	s_mov_b32 m0, s42
	v_lshl_add_u64 v[232:233], s[0:1], 0, v[130:131]
	ds_read_b128 v[188:191], v154 offset:32768
	ds_read_b128 v[192:195], v154 offset:33792
	ds_read_b128 v[196:199], v154 offset:34816
	ds_read_b128 v[200:203], v154 offset:35840
	ds_read_b128 v[204:207], v154 offset:36864
	ds_read_b128 v[212:215], v154 offset:37888
	ds_read_b128 v[216:219], v154 offset:38912
	ds_read_b128 v[220:223], v154 offset:39936
	s_mov_b32 m0, s40
	s_nop 0
	global_load_lds_dwordx4 v[228:229], off
	s_mov_b32 m0, s41
	s_nop 0
	global_load_lds_dwordx4 v[230:231], off
	s_mov_b32 m0, s42
	s_nop 0
	global_load_lds_dwordx4 v[232:233], off
	v_lshl_add_u64 v[232:233], s[0:1], 0, v[134:135]
	s_mov_b32 m0, s43
	s_nop 0
	global_load_lds_dwordx4 v[232:233], off
	s_waitcnt vmcnt(8)
	s_waitcnt lgkmcnt(0)
	s_barrier
	s_setprio 1
	s_waitcnt lgkmcnt(0)
	v_mfma_f32_16x16x32_bf16 v[126:129], v[156:159], v[188:191], v[126:129]
	v_mfma_f32_16x16x32_bf16 v[122:125], v[164:167], v[188:191], v[122:125]
	v_mfma_f32_16x16x32_bf16 v[110:113], v[156:159], v[196:199], v[110:113]
	v_mfma_f32_16x16x32_bf16 v[106:109], v[164:167], v[196:199], v[106:109]
	v_mfma_f32_16x16x32_bf16 v[94:97], v[156:159], v[204:207], v[94:97]
	v_mfma_f32_16x16x32_bf16 v[90:93], v[164:167], v[204:207], v[90:93]
	v_mfma_f32_16x16x32_bf16 v[78:81], v[156:159], v[216:219], v[78:81]
	v_mfma_f32_16x16x32_bf16 v[74:77], v[164:167], v[216:219], v[74:77]
	v_mfma_f32_16x16x32_bf16 v[126:129], v[160:163], v[192:195], v[126:129]
	v_mfma_f32_16x16x32_bf16 v[122:125], v[168:171], v[192:195], v[122:125]
	v_mfma_f32_16x16x32_bf16 v[110:113], v[160:163], v[200:203], v[110:113]
	v_mfma_f32_16x16x32_bf16 v[106:109], v[168:171], v[200:203], v[106:109]
	v_mfma_f32_16x16x32_bf16 v[94:97], v[160:163], v[212:215], v[94:97]
	v_mfma_f32_16x16x32_bf16 v[90:93], v[168:171], v[212:215], v[90:93]
	v_mfma_f32_16x16x32_bf16 v[78:81], v[160:163], v[220:223], v[78:81]
	v_mfma_f32_16x16x32_bf16 v[74:77], v[168:171], v[220:223], v[74:77]
	v_mfma_f32_16x16x32_bf16 v[118:121], v[172:175], v[188:191], v[118:121]
	v_mfma_f32_16x16x32_bf16 v[114:117], v[180:183], v[188:191], v[114:117]
	v_mfma_f32_16x16x32_bf16 v[102:105], v[172:175], v[196:199], v[102:105]
	v_mfma_f32_16x16x32_bf16 v[98:101], v[180:183], v[196:199], v[98:101]
	v_mfma_f32_16x16x32_bf16 v[86:89], v[172:175], v[204:207], v[86:89]
	v_mfma_f32_16x16x32_bf16 v[82:85], v[180:183], v[204:207], v[82:85]
	v_mfma_f32_16x16x32_bf16 v[70:73], v[172:175], v[216:219], v[70:73]
	v_mfma_f32_16x16x32_bf16 v[66:69], v[180:183], v[216:219], v[66:69]
	v_mfma_f32_16x16x32_bf16 v[118:121], v[176:179], v[192:195], v[118:121]
	v_mfma_f32_16x16x32_bf16 v[114:117], v[184:187], v[192:195], v[114:117]
	v_mfma_f32_16x16x32_bf16 v[102:105], v[176:179], v[200:203], v[102:105]
	v_mfma_f32_16x16x32_bf16 v[98:101], v[184:187], v[200:203], v[98:101]
	v_mfma_f32_16x16x32_bf16 v[86:89], v[176:179], v[212:215], v[86:89]
	v_mfma_f32_16x16x32_bf16 v[82:85], v[184:187], v[212:215], v[82:85]
	v_mfma_f32_16x16x32_bf16 v[70:73], v[176:179], v[220:223], v[70:73]
	v_mfma_f32_16x16x32_bf16 v[66:69], v[184:187], v[220:223], v[66:69]
	s_setprio 0
	s_barrier
	s_add_i32 s0, s33, s39
	s_add_i32 m0, s0, 0xffffff80
	ds_read_b128 v[188:191], v154 offset:49152
	ds_read_b128 v[192:195], v154 offset:50176
	ds_read_b128 v[196:199], v154 offset:51200
	ds_read_b128 v[200:203], v154 offset:52224
	ds_read_b128 v[204:207], v154 offset:53248
	ds_read_b128 v[212:215], v154 offset:54272
	ds_read_b128 v[216:219], v154 offset:55296
	ds_read_b128 v[220:223], v154 offset:56320
	global_load_lds_dwordx4 v[148:149], off offset:128
	s_add_i32 m0, s0, 0x1f80
	s_add_i32 s0, s63, s39
	global_load_lds_dwordx4 v[208:209], off offset:128
	s_add_i32 m0, s0, 0xffffff80
	s_nop 0
	global_load_lds_dwordx4 v[224:225], off offset:128
	s_add_i32 m0, s0, 0x1f80
	s_nop 0
	global_load_lds_dwordx4 v[226:227], off offset:128
	s_cmp_ge_i32 s61, s48
	s_cbranch_scc0 .Lkr4_b
	s_add_i32 m0, s46, 0xffffff80
	s_nop 0
	global_load_lds_dwordx4 v[228:229], off offset:128
	s_add_i32 m0, s47, 0xffffff80
	s_nop 0
	global_load_lds_dwordx4 v[230:231], off offset:128

; #define PG8_STAGE(bufoff, gbase, voff) do { _Pragma("unroll") for (int _i = 0; _i < 2; ++_i) \
;         __builtin_amdgcn_global_load_lds((const unsigned*)((const char*)(gbase) + (voff)[_i]), (PG8_LAS unsigned*)(lds + (bufoff) + ldsw + _i * 8192), 16, 0, 0); } while (0)
; #define PG8_LDA(dst, b, h) do { _Pragma("unroll") for (int m = 0; m < 4; ++m) { const bf16x8 f0_ = *(const PG8_LAS bf16x8*)(lds + PG8_SA(b, h) + aoff + m * 2048), f1_ = *(const PG8_LAS bf16x8*)(lds + PG8_SA(b, h) + aoff + m * 2048 + 1024); dst[m].set(f0_, f1_); } } while (0)
; #define PG8_LDB(dst, b, h) do { _Pragma("unroll") for (int n = 0; n < 2; ++n) { const bf16x8 f0_ = *(const PG8_LAS bf16x8*)(lds + PG8_SB(b, h) + boff + n * 2048), f1_ = *(const PG8_LAS bf16x8*)(lds + PG8_SB(b, h) + boff + n * 2048 + 1024); dst[n].set(f0_, f1_); } } while (0)
; #define PG8_WAIT_V(n) asm volatile("s_waitcnt vmcnt(" #n ")" ::: "memory")
; #define PG8_WAIT_L(n) asm volatile("s_waitcnt lgkmcnt(" #n ")" ::: "memory")
; #define PG8_BAR __builtin_amdgcn_s_barrier()
; #define PG8_SCHED __builtin_amdgcn_sched_barrier(0)
; template <class Epi, class Sched, bool ALIGN_EPI = false, bool SP2 = false>
; __device__ __forceinline__ void gemm_phase(PG8_LAS unsigned char* lds, const Gemm g, const Sched& S, const Epi& E) {
;     ...
;             PG8_LDB(B0, 0, 0); PG8_LDB(B1, 0, 1); PG8_SCHED; PG8_LDA(At, 0, 0); PG8_STAGE(PG8_SA(1, 1), a1 + hstep, voffA);
;             PG8_WAIT_V(8); PG8_WAIT_L(0); PG8_BAR; PG8_MMA(0, 0, At, B0); PG8_MMA(0, 1, At, B1); PG8_BAR; PG8_SCHED;
;             PG8_LDA(At, 0, 1); PG8_STAGE(PG8_SB(0, 0), b2, voffB); PG8_STAGE(PG8_SB(0, 1), b2 + hstepB, voffB); PG8_STAGE(PG8_SA(0, 0), a2, voffA);
;             PG8_WAIT_V(8); PG8_WAIT_L(0); PG8_BAR; PG8_MMA(1, 0, At, B0); PG8_MMA(1, 1, At, B1); PG8_BAR; PG8_SCHED;
.Lkr5_a:
	v_lshl_add_u64 v[192:193], s[46:47], 0, v[176:177]
	s_add_i32 m0, s10, 0xc000
	ds_read_b128 v[184:187], v199
	ds_read_b128 v[188:191], v199 offset:1024
	ds_read_b128 v[212:215], v199 offset:2048
	ds_read_b128 v[216:219], v199 offset:3072
	ds_read_b128 v[220:223], v199 offset:4096
	ds_read_b128 v[224:227], v199 offset:5120
	ds_read_b128 v[228:231], v199 offset:6144
	ds_read_b128 v[232:235], v199 offset:7168
	global_load_lds_dwordx4 v[192:193], off
	v_lshl_add_u64 v[192:193], s[46:47], 0, v[178:179]
	s_add_i32 m0, s10, 0xe000
	s_nop 0
	global_load_lds_dwordx4 v[192:193], off
	s_waitcnt vmcnt(8)
	s_waitcnt lgkmcnt(0)
	s_barrier
	s_setprio 1
	s_waitcnt lgkmcnt(0)
	v_mfma_scale_f32_16x16x128_f8f6f4 v[158:161], v[18:25], v[184:191], v[158:161], v200, v201 op_sel_hi:[0,0,0]
	v_mfma_scale_f32_16x16x128_f8f6f4 v[154:157], v[26:33], v[184:191], v[154:157], v200, v201 op_sel_hi:[0,0,0]
	v_mfma_scale_f32_16x16x128_f8f6f4 v[142:145], v[18:25], v[212:219], v[142:145], v200, v201 op_sel_hi:[0,0,0]
	v_mfma_scale_f32_16x16x128_f8f6f4 v[138:141], v[26:33], v[212:219], v[138:141], v200, v201 op_sel_hi:[0,0,0]
	v_mfma_scale_f32_16x16x128_f8f6f4 v[126:129], v[18:25], v[220:227], v[126:129], v200, v201 op_sel_hi:[0,0,0]
	v_mfma_scale_f32_16x16x128_f8f6f4 v[122:125], v[26:33], v[220:227], v[122:125], v200, v201 op_sel_hi:[0,0,0]
	v_mfma_scale_f32_16x16x128_f8f6f4 v[110:113], v[18:25], v[228:235], v[110:113], v200, v201 op_sel_hi:[0,0,0]
	v_mfma_scale_f32_16x16x128_f8f6f4 v[106:109], v[26:33], v[228:235], v[106:109], v200, v201 op_sel_hi:[0,0,0]
	v_mfma_scale_f32_16x16x128_f8f6f4 v[150:153], v[2:9], v[184:191], v[150:153], v200, v201 op_sel_hi:[0,0,0]
	v_mfma_scale_f32_16x16x128_f8f6f4 v[146:149], v[10:17], v[184:191], v[146:149], v200, v201 op_sel_hi:[0,0,0]
	v_mfma_scale_f32_16x16x128_f8f6f4 v[134:137], v[2:9], v[212:219], v[134:137], v200, v201 op_sel_hi:[0,0,0]
	v_mfma_scale_f32_16x16x128_f8f6f4 v[130:133], v[10:17], v[212:219], v[130:133], v200, v201 op_sel_hi:[0,0,0]
	v_mfma_scale_f32_16x16x128_f8f6f4 v[118:121], v[2:9], v[220:227], v[118:121], v200, v201 op_sel_hi:[0,0,0]
	v_mfma_scale_f32_16x16x128_f8f6f4 v[114:117], v[10:17], v[220:227], v[114:117], v200, v201 op_sel_hi:[0,0,0]
	v_mfma_scale_f32_16x16x128_f8f6f4 v[102:105], v[2:9], v[228:235], v[102:105], v200, v201 op_sel_hi:[0,0,0]
	v_mfma_scale_f32_16x16x128_f8f6f4 v[98:101], v[10:17], v[228:235], v[98:101], v200, v201 op_sel_hi:[0,0,0]
	s_setprio 0
	s_barrier
	s_add_i32 s0, s73, s9
	v_lshl_add_u64 v[184:185], s[50:51], 0, v[164:165]
	s_mov_b32 m0, s0
	ds_read_b128 v[212:215], v199 offset:16384
	ds_read_b128 v[216:219], v199 offset:17408
	ds_read_b128 v[220:223], v199 offset:18432
	ds_read_b128 v[224:227], v199 offset:19456
	ds_read_b128 v[228:231], v199 offset:20480
	ds_read_b128 v[232:235], v199 offset:21504
	ds_read_b128 v[236:239], v199 offset:22528
	ds_read_b128 v[240:243], v199 offset:23552
	global_load_lds_dwordx4 v[184:185], off
	s_add_i32 m0, s0, 0x2000
	s_add_u32 s0, s50, s14
	v_lshl_add_u64 v[186:187], s[50:51], 0, v[168:169]
	s_addc_u32 s1, s51, s15
	s_add_i32 s33, s74, s9
	global_load_lds_dwordx4 v[186:187], off
	v_lshl_add_u64 v[188:189], s[0:1], 0, v[164:165]
	s_mov_b32 m0, s33
	v_lshl_add_u64 v[190:191], s[0:1], 0, v[168:169]
	global_load_lds_dwordx4 v[188:189], off
	s_add_i32 m0, s33, 0x2000
	v_lshl_add_u64 v[192:193], s[48:49], 0, v[162:163]
	global_load_lds_dwordx4 v[190:191], off
	v_lshl_add_u64 v[194:195], s[48:49], 0, v[166:167]
	s_waitcnt vmcnt(6)
	s_waitcnt lgkmcnt(0)
	s_barrier
	s_setprio 1
	s_waitcnt lgkmcnt(0)
	v_mfma_scale_f32_16x16x128_f8f6f4 v[94:97], v[18:25], v[212:219], v[94:97], v200, v201 op_sel_hi:[0,0,0]
	v_mfma_scale_f32_16x16x128_f8f6f4 v[90:93], v[26:33], v[212:219], v[90:93], v200, v201 op_sel_hi:[0,0,0]
	v_mfma_scale_f32_16x16x128_f8f6f4 v[78:81], v[18:25], v[220:227], v[78:81], v200, v201 op_sel_hi:[0,0,0]
	v_mfma_scale_f32_16x16x128_f8f6f4 v[74:77], v[26:33], v[220:227], v[74:77], v200, v201 op_sel_hi:[0,0,0]
	v_mfma_scale_f32_16x16x128_f8f6f4 v[62:65], v[18:25], v[228:235], v[62:65], v200, v201 op_sel_hi:[0,0,0]
	v_mfma_scale_f32_16x16x128_f8f6f4 v[58:61], v[26:33], v[228:235], v[58:61], v200, v201 op_sel_hi:[0,0,0]
	v_mfma_scale_f32_16x16x128_f8f6f4 v[46:49], v[18:25], v[236:243], v[46:49], v200, v201 op_sel_hi:[0,0,0]
	v_mfma_scale_f32_16x16x128_f8f6f4 v[42:45], v[26:33], v[236:243], v[42:45], v200, v201 op_sel_hi:[0,0,0]
	v_mfma_scale_f32_16x16x128_f8f6f4 v[86:89], v[2:9], v[212:219], v[86:89], v200, v201 op_sel_hi:[0,0,0]
	v_mfma_scale_f32_16x16x128_f8f6f4 v[82:85], v[10:17], v[212:219], v[82:85], v200, v201 op_sel_hi:[0,0,0]
	v_mfma_scale_f32_16x16x128_f8f6f4 v[70:73], v[2:9], v[220:227], v[70:73], v200, v201 op_sel_hi:[0,0,0]
	v_mfma_scale_f32_16x16x128_f8f6f4 v[66:69], v[10:17], v[220:227], v[66:69], v200, v201 op_sel_hi:[0,0,0]
	v_mfma_scale_f32_16x16x128_f8f6f4 v[54:57], v[2:9], v[228:235], v[54:57], v200, v201 op_sel_hi:[0,0,0]
	v_mfma_scale_f32_16x16x128_f8f6f4 v[50:53], v[10:17], v[228:235], v[50:53], v200, v201 op_sel_hi:[0,0,0]
	v_mfma_scale_f32_16x16x128_f8f6f4 v[38:41], v[2:9], v[236:243], v[38:41], v200, v201 op_sel_hi:[0,0,0]
	v_mfma_scale_f32_16x16x128_f8f6f4 v[34:37], v[10:17], v[236:243], v[34:37], v200, v201 op_sel_hi:[0,0,0]
	s_setprio 0
	s_barrier
; #define PG8_STAGE(bufoff, gbase, voff) do { _Pragma("unroll") for (int _i = 0; _i < 2; ++_i) \
;         __builtin_amdgcn_global_load_lds((const unsigned*)((const char*)(gbase) + (voff)[_i]), (PG8_LAS unsigned*)(lds + (bufoff) + ldsw + _i * 8192), 16, 0, 0); } while (0)
; #define PG8_LDA(dst, b, h) do { _Pragma("unroll") for (int m = 0; m < 4; ++m) { const bf16x8 f0_ = *(const PG8_LAS bf16x8*)(lds + PG8_SA(b, h) + aoff + m * 2048), f1_ = *(const PG8_LAS bf16x8*)(lds + PG8_SA(b, h) + aoff + m * 2048 + 1024); dst[m].set(f0_, f1_); } } while (0)
; #define PG8_LDB(dst, b, h) do { _Pragma("unroll") for (int n = 0; n < 2; ++n) { const bf16x8 f0_ = *(const PG8_LAS bf16x8*)(lds + PG8_SB(b, h) + boff + n * 2048), f1_ = *(const PG8_LAS bf16x8*)(lds + PG8_SB(b, h) + boff + n * 2048 + 1024); dst[n].set(f0_, f1_); } } while (0)
; #define PG8_WAIT_V(n) asm volatile("s_waitcnt vmcnt(" #n ")" ::: "memory")
; #define PG8_WAIT_L(n) asm volatile("s_waitcnt lgkmcnt(" #n ")" ::: "memory")
; #define PG8_BAR __builtin_amdgcn_s_barrier()
; #define PG8_SCHED __builtin_amdgcn_sched_barrier(0)
; template <class Epi, class Sched, bool ALIGN_EPI = false, bool SP2 = false>
; __device__ __forceinline__ void gemm_phase(PG8_LAS unsigned char* lds, const Gemm g, const Sched& S, const Epi& E) {
;     ...
;             PG8_LDB(B0, 1, 0); PG8_LDB(B1, 1, 1); PG8_SCHED; PG8_LDA(At, 1, 0); PG8_STAGE(PG8_SA(0, 1), a2 + hstep, voffA);
;             PG8_WAIT_V(8); PG8_WAIT_L(0); PG8_BAR; PG8_MMA(0, 0, At, B0); PG8_MMA(0, 1, At, B1); PG8_BAR; PG8_SCHED;
;             PG8_LDA(At, 1, 1); PG8_STAGE(PG8_SB(1, 0), b3, voffB); PG8_STAGE(PG8_SB(1, 1), b3 + hstepB, voffB); PG8_STAGE(PG8_SA(1, 0), a3, voffA);
	s_add_i32 s33, 0, 0x18000
	s_add_i32 s50, 0, 0x1c000
	v_add_u32_e32 v14, s33, v173
	v_add_u32_e32 v30, s50, v173
	ds_read_b128 v[2:5], v14
	ds_read_b128 v[6:9], v14 offset:1024
	ds_read_b128 v[10:13], v14 offset:2048
	ds_read_b128 v[14:17], v14 offset:3072
	ds_read_b128 v[18:21], v30
	ds_read_b128 v[22:25], v30 offset:1024
	ds_read_b128 v[26:29], v30 offset:2048
	ds_read_b128 v[30:33], v30 offset:3072
	s_add_u32 s0, s48, s12
	s_addc_u32 s1, s49, s13
	s_mov_b32 m0, s52
	v_lshl_add_u64 v[204:205], s[0:1], 0, v[162:163]
	ds_read_b128 v[212:215], v199 offset:32768
	ds_read_b128 v[216:219], v199 offset:33792
	ds_read_b128 v[220:223], v199 offset:34816
	ds_read_b128 v[224:227], v199 offset:35840
	ds_read_b128 v[228:231], v199 offset:36864
	ds_read_b128 v[232:235], v199 offset:37888
	ds_read_b128 v[236:239], v199 offset:38912
	ds_read_b128 v[240:243], v199 offset:39936
	s_mov_b32 m0, s10
	s_nop 0
	global_load_lds_dwordx4 v[192:193], off
	s_mov_b32 m0, s11
	s_nop 0
	global_load_lds_dwordx4 v[194:195], off
	s_mov_b32 m0, s52
	s_nop 0
	global_load_lds_dwordx4 v[204:205], off
	v_lshl_add_u64 v[204:205], s[0:1], 0, v[166:167]
	s_mov_b32 m0, s53
	s_nop 0
	global_load_lds_dwordx4 v[204:205], off
	s_waitcnt vmcnt(8)
	s_waitcnt lgkmcnt(0)
	s_barrier
	s_setprio 1
	s_waitcnt lgkmcnt(0)
	v_mfma_scale_f32_16x16x128_f8f6f4 v[158:161], v[2:9], v[212:219], v[158:161], v200, v201 op_sel_hi:[0,0,0]
	v_mfma_scale_f32_16x16x128_f8f6f4 v[154:157], v[10:17], v[212:219], v[154:157], v200, v201 op_sel_hi:[0,0,0]
	v_mfma_scale_f32_16x16x128_f8f6f4 v[142:145], v[2:9], v[220:227], v[142:145], v200, v201 op_sel_hi:[0,0,0]
	v_mfma_scale_f32_16x16x128_f8f6f4 v[138:141], v[10:17], v[220:227], v[138:141], v200, v201 op_sel_hi:[0,0,0]
	v_mfma_scale_f32_16x16x128_f8f6f4 v[126:129], v[2:9], v[228:235], v[126:129], v200, v201 op_sel_hi:[0,0,0]
	v_mfma_scale_f32_16x16x128_f8f6f4 v[122:125], v[10:17], v[228:235], v[122:125], v200, v201 op_sel_hi:[0,0,0]
	v_mfma_scale_f32_16x16x128_f8f6f4 v[110:113], v[2:9], v[236:243], v[110:113], v200, v201 op_sel_hi:[0,0,0]
	v_mfma_scale_f32_16x16x128_f8f6f4 v[106:109], v[10:17], v[236:243], v[106:109], v200, v201 op_sel_hi:[0,0,0]
	v_mfma_scale_f32_16x16x128_f8f6f4 v[150:153], v[18:25], v[212:219], v[150:153], v200, v201 op_sel_hi:[0,0,0]
	v_mfma_scale_f32_16x16x128_f8f6f4 v[146:149], v[26:33], v[212:219], v[146:149], v200, v201 op_sel_hi:[0,0,0]
	v_mfma_scale_f32_16x16x128_f8f6f4 v[134:137], v[18:25], v[220:227], v[134:137], v200, v201 op_sel_hi:[0,0,0]
	v_mfma_scale_f32_16x16x128_f8f6f4 v[130:133], v[26:33], v[220:227], v[130:133], v200, v201 op_sel_hi:[0,0,0]
	v_mfma_scale_f32_16x16x128_f8f6f4 v[118:121], v[18:25], v[228:235], v[118:121], v200, v201 op_sel_hi:[0,0,0]
	v_mfma_scale_f32_16x16x128_f8f6f4 v[114:117], v[26:33], v[228:235], v[114:117], v200, v201 op_sel_hi:[0,0,0]
	v_mfma_scale_f32_16x16x128_f8f6f4 v[102:105], v[18:25], v[236:243], v[102:105], v200, v201 op_sel_hi:[0,0,0]
	v_mfma_scale_f32_16x16x128_f8f6f4 v[98:101], v[26:33], v[236:243], v[98:101], v200, v201 op_sel_hi:[0,0,0]
	s_setprio 0
	s_barrier
	s_add_i32 s0, s33, s9
	s_add_i32 m0, s0, 0xffffff80
	ds_read_b128 v[212:215], v199 offset:49152
	ds_read_b128 v[216:219], v199 offset:50176
	ds_read_b128 v[220:223], v199 offset:51200
	ds_read_b128 v[224:227], v199 offset:52224
	ds_read_b128 v[228:231], v199 offset:53248
	ds_read_b128 v[232:235], v199 offset:54272
	ds_read_b128 v[236:239], v199 offset:55296
	ds_read_b128 v[240:243], v199 offset:56320
	global_load_lds_dwordx4 v[184:185], off offset:128
	s_add_i32 m0, s0, 0x1f80
	s_add_i32 s0, s50, s9
	global_load_lds_dwordx4 v[186:187], off offset:128
	s_add_i32 m0, s0, 0xffffff80
	s_nop 0
	global_load_lds_dwordx4 v[188:189], off offset:128
	s_add_i32 m0, s0, 0x1f80
	s_nop 0
	global_load_lds_dwordx4 v[190:191], off offset:128
	s_cmp_ge_i32 s82, s58
	s_cbranch_scc0 .Lkr5_b
	s_add_i32 m0, s56, 0xffffff80
	s_nop 0
	global_load_lds_dwordx4 v[192:193], off offset:128
	s_add_i32 m0, s57, 0xffffff80
	s_nop 0
	global_load_lds_dwordx4 v[194:195], off offset:128

; #define PG8_STAGE(bufoff, gbase, voff) do { _Pragma("unroll") for (int _i = 0; _i < 2; ++_i) \
;         __builtin_amdgcn_global_load_lds((const unsigned*)((const char*)(gbase) + (voff)[_i]), (PG8_LAS unsigned*)(lds + (bufoff) + ldsw + _i * 8192), 16, 0, 0); } while (0)
; #define PG8_LDA(dst, b, h) do { _Pragma("unroll") for (int m = 0; m < 4; ++m) { const bf16x8 f0_ = *(const PG8_LAS bf16x8*)(lds + PG8_SA(b, h) + aoff + m * 2048), f1_ = *(const PG8_LAS bf16x8*)(lds + PG8_SA(b, h) + aoff + m * 2048 + 1024); dst[m].set(f0_, f1_); } } while (0)
; #define PG8_LDB(dst, b, h) do { _Pragma("unroll") for (int n = 0; n < 2; ++n) { const bf16x8 f0_ = *(const PG8_LAS bf16x8*)(lds + PG8_SB(b, h) + boff + n * 2048), f1_ = *(const PG8_LAS bf16x8*)(lds + PG8_SB(b, h) + boff + n * 2048 + 1024); dst[n].set(f0_, f1_); } } while (0)
; #define PG8_WAIT_V(n) asm volatile("s_waitcnt vmcnt(" #n ")" ::: "memory")
; #define PG8_WAIT_L(n) asm volatile("s_waitcnt lgkmcnt(" #n ")" ::: "memory")
; #define PG8_BAR __builtin_amdgcn_s_barrier()
; #define PG8_SCHED __builtin_amdgcn_sched_barrier(0)
; template <class Epi, class Sched, bool ALIGN_EPI = false, bool SP2 = false>
; __device__ __forceinline__ void gemm_phase(PG8_LAS unsigned char* lds, const Gemm g, const Sched& S, const Epi& E) {
;     ...
;             PG8_LDB(B0, 0, 0); PG8_LDB(B1, 0, 1); PG8_SCHED; PG8_LDA(At, 0, 0); PG8_STAGE(PG8_SA(1, 1), a1 + hstep, voffA);
;             PG8_WAIT_V(8); PG8_WAIT_L(0); PG8_BAR; PG8_MMA(0, 0, At, B0); PG8_MMA(0, 1, At, B1); PG8_BAR; PG8_SCHED;
;             PG8_LDA(At, 0, 1); PG8_STAGE(PG8_SB(0, 0), b2, voffB); PG8_STAGE(PG8_SB(0, 1), b2 + hstepB, voffB); PG8_STAGE(PG8_SA(0, 0), a2, voffA);
;             PG8_WAIT_V(8); PG8_WAIT_L(0); PG8_BAR; PG8_MMA(1, 0, At, B0); PG8_MMA(1, 1, At, B1); PG8_BAR; PG8_SCHED;
.Lkr6_a:
	v_lshl_add_u64 v[206:207], s[2:3], 0, v[198:199]
	s_add_i32 m0, s71, 0xc000
	ds_read_b128 v[152:155], v217
	ds_read_b128 v[156:159], v217 offset:1024
	ds_read_b128 v[168:171], v217 offset:2048
	ds_read_b128 v[172:175], v217 offset:3072
	ds_read_b128 v[176:179], v217 offset:4096
	ds_read_b128 v[180:183], v217 offset:5120
	ds_read_b128 v[226:229], v217 offset:6144
	ds_read_b128 v[230:233], v217 offset:7168
	global_load_lds_dwordx4 v[206:207], off
	v_lshl_add_u64 v[206:207], s[2:3], 0, v[200:201]
	s_add_i32 m0, s71, 0xe000
	s_nop 0
	global_load_lds_dwordx4 v[206:207], off
	s_waitcnt vmcnt(8)
	s_waitcnt lgkmcnt(0)
	s_barrier
	s_setprio 1
	s_waitcnt lgkmcnt(0)
	v_mfma_scale_f32_16x16x128_f8f6f4 v[164:167], v[16:23], v[152:159], v[164:167], v218, v219 op_sel_hi:[0,0,0]
	v_mfma_scale_f32_16x16x128_f8f6f4 v[160:163], v[24:31], v[152:159], v[160:163], v218, v219 op_sel_hi:[0,0,0]
	v_mfma_scale_f32_16x16x128_f8f6f4 v[140:143], v[16:23], v[168:175], v[140:143], v218, v219 op_sel_hi:[0,0,0]
	v_mfma_scale_f32_16x16x128_f8f6f4 v[136:139], v[24:31], v[168:175], v[136:139], v218, v219 op_sel_hi:[0,0,0]
	v_mfma_scale_f32_16x16x128_f8f6f4 v[108:111], v[16:23], v[176:183], v[108:111], v218, v219 op_sel_hi:[0,0,0]
	v_mfma_scale_f32_16x16x128_f8f6f4 v[104:107], v[24:31], v[176:183], v[104:107], v218, v219 op_sel_hi:[0,0,0]
	v_mfma_scale_f32_16x16x128_f8f6f4 v[116:119], v[16:23], v[226:233], v[116:119], v218, v219 op_sel_hi:[0,0,0]
	v_mfma_scale_f32_16x16x128_f8f6f4 v[112:115], v[24:31], v[226:233], v[112:115], v218, v219 op_sel_hi:[0,0,0]
	v_mfma_scale_f32_16x16x128_f8f6f4 v[148:151], v[0:7], v[152:159], v[148:151], v218, v219 op_sel_hi:[0,0,0]
	v_mfma_scale_f32_16x16x128_f8f6f4 v[144:147], v[8:15], v[152:159], v[144:147], v218, v219 op_sel_hi:[0,0,0]
	v_mfma_scale_f32_16x16x128_f8f6f4 v[132:135], v[0:7], v[168:175], v[132:135], v218, v219 op_sel_hi:[0,0,0]
	v_mfma_scale_f32_16x16x128_f8f6f4 v[128:131], v[8:15], v[168:175], v[128:131], v218, v219 op_sel_hi:[0,0,0]
	v_mfma_scale_f32_16x16x128_f8f6f4 v[124:127], v[0:7], v[176:183], v[124:127], v218, v219 op_sel_hi:[0,0,0]
	v_mfma_scale_f32_16x16x128_f8f6f4 v[120:123], v[8:15], v[176:183], v[120:123], v218, v219 op_sel_hi:[0,0,0]
	v_mfma_scale_f32_16x16x128_f8f6f4 v[100:103], v[0:7], v[226:233], v[100:103], v218, v219 op_sel_hi:[0,0,0]
	v_mfma_scale_f32_16x16x128_f8f6f4 v[96:99], v[8:15], v[226:233], v[96:99], v218, v219 op_sel_hi:[0,0,0]
	s_setprio 0
	s_barrier
	s_add_i32 s0, s67, s45
	v_lshl_add_u64 v[152:153], s[80:81], 0, v[186:187]
	s_mov_b32 m0, s0
	ds_read_b128 v[172:175], v217 offset:16384
	ds_read_b128 v[176:179], v217 offset:17408
	ds_read_b128 v[226:229], v217 offset:18432
	ds_read_b128 v[230:233], v217 offset:19456
	ds_read_b128 v[234:237], v217 offset:20480
	ds_read_b128 v[238:241], v217 offset:21504
	ds_read_b128 v[242:245], v217 offset:22528
	ds_read_b128 v[246:249], v217 offset:23552
	global_load_lds_dwordx4 v[152:153], off
	s_add_i32 m0, s0, 0x2000
	s_add_u32 s0, s80, s20
	v_lshl_add_u64 v[154:155], s[80:81], 0, v[190:191]
	s_addc_u32 s1, s81, s21
	s_add_i32 s33, s10, s45
	global_load_lds_dwordx4 v[154:155], off
	v_lshl_add_u64 v[156:157], s[0:1], 0, v[186:187]
	s_mov_b32 m0, s33
	v_lshl_add_u64 v[158:159], s[0:1], 0, v[190:191]
	global_load_lds_dwordx4 v[156:157], off
	s_add_i32 m0, s33, 0x2000
	v_lshl_add_u64 v[168:169], s[78:79], 0, v[184:185]
	global_load_lds_dwordx4 v[158:159], off
	v_lshl_add_u64 v[170:171], s[78:79], 0, v[188:189]
	s_waitcnt vmcnt(6)
	s_waitcnt lgkmcnt(0)
	s_barrier
	s_setprio 1
	s_waitcnt lgkmcnt(0)
	v_mfma_scale_f32_16x16x128_f8f6f4 v[92:95], v[16:23], v[172:179], v[92:95], v218, v219 op_sel_hi:[0,0,0]
	v_mfma_scale_f32_16x16x128_f8f6f4 v[88:91], v[24:31], v[172:179], v[88:91], v218, v219 op_sel_hi:[0,0,0]
	v_mfma_scale_f32_16x16x128_f8f6f4 v[76:79], v[16:23], v[226:233], v[76:79], v218, v219 op_sel_hi:[0,0,0]
	v_mfma_scale_f32_16x16x128_f8f6f4 v[72:75], v[24:31], v[226:233], v[72:75], v218, v219 op_sel_hi:[0,0,0]
	v_mfma_scale_f32_16x16x128_f8f6f4 v[60:63], v[16:23], v[234:241], v[60:63], v218, v219 op_sel_hi:[0,0,0]
	v_mfma_scale_f32_16x16x128_f8f6f4 v[56:59], v[24:31], v[234:241], v[56:59], v218, v219 op_sel_hi:[0,0,0]
	v_mfma_scale_f32_16x16x128_f8f6f4 v[44:47], v[16:23], v[242:249], v[44:47], v218, v219 op_sel_hi:[0,0,0]
	v_mfma_scale_f32_16x16x128_f8f6f4 v[40:43], v[24:31], v[242:249], v[40:43], v218, v219 op_sel_hi:[0,0,0]
	v_mfma_scale_f32_16x16x128_f8f6f4 v[84:87], v[0:7], v[172:179], v[84:87], v218, v219 op_sel_hi:[0,0,0]
	v_mfma_scale_f32_16x16x128_f8f6f4 v[80:83], v[8:15], v[172:179], v[80:83], v218, v219 op_sel_hi:[0,0,0]
	v_mfma_scale_f32_16x16x128_f8f6f4 v[68:71], v[0:7], v[226:233], v[68:71], v218, v219 op_sel_hi:[0,0,0]
	v_mfma_scale_f32_16x16x128_f8f6f4 v[64:67], v[8:15], v[226:233], v[64:67], v218, v219 op_sel_hi:[0,0,0]
	v_mfma_scale_f32_16x16x128_f8f6f4 v[52:55], v[0:7], v[234:241], v[52:55], v218, v219 op_sel_hi:[0,0,0]
	v_mfma_scale_f32_16x16x128_f8f6f4 v[48:51], v[8:15], v[234:241], v[48:51], v218, v219 op_sel_hi:[0,0,0]
	v_mfma_scale_f32_16x16x128_f8f6f4 v[36:39], v[0:7], v[242:249], v[36:39], v218, v219 op_sel_hi:[0,0,0]
	v_mfma_scale_f32_16x16x128_f8f6f4 v[32:35], v[8:15], v[242:249], v[32:35], v218, v219 op_sel_hi:[0,0,0]
	s_setprio 0
	s_barrier
; #define PG8_STAGE(bufoff, gbase, voff) do { _Pragma("unroll") for (int _i = 0; _i < 2; ++_i) \
;         __builtin_amdgcn_global_load_lds((const unsigned*)((const char*)(gbase) + (voff)[_i]), (PG8_LAS unsigned*)(lds + (bufoff) + ldsw + _i * 8192), 16, 0, 0); } while (0)
; #define PG8_LDA(dst, b, h) do { _Pragma("unroll") for (int m = 0; m < 4; ++m) { const bf16x8 f0_ = *(const PG8_LAS bf16x8*)(lds + PG8_SA(b, h) + aoff + m * 2048), f1_ = *(const PG8_LAS bf16x8*)(lds + PG8_SA(b, h) + aoff + m * 2048 + 1024); dst[m].set(f0_, f1_); } } while (0)
; #define PG8_LDB(dst, b, h) do { _Pragma("unroll") for (int n = 0; n < 2; ++n) { const bf16x8 f0_ = *(const PG8_LAS bf16x8*)(lds + PG8_SB(b, h) + boff + n * 2048), f1_ = *(const PG8_LAS bf16x8*)(lds + PG8_SB(b, h) + boff + n * 2048 + 1024); dst[n].set(f0_, f1_); } } while (0)
; #define PG8_WAIT_V(n) asm volatile("s_waitcnt vmcnt(" #n ")" ::: "memory")
; #define PG8_WAIT_L(n) asm volatile("s_waitcnt lgkmcnt(" #n ")" ::: "memory")
; #define PG8_BAR __builtin_amdgcn_s_barrier()
; #define PG8_SCHED __builtin_amdgcn_sched_barrier(0)
; template <class Epi, class Sched, bool ALIGN_EPI = false, bool SP2 = false>
; __device__ __forceinline__ void gemm_phase(PG8_LAS unsigned char* lds, const Gemm g, const Sched& S, const Epi& E) {
;     ...
;             PG8_LDB(B0, 1, 0); PG8_LDB(B1, 1, 1); PG8_SCHED; PG8_LDA(At, 1, 0); PG8_STAGE(PG8_SA(0, 1), a2 + hstep, voffA);
;             PG8_WAIT_V(8); PG8_WAIT_L(0); PG8_BAR; PG8_MMA(0, 0, At, B0); PG8_MMA(0, 1, At, B1); PG8_BAR; PG8_SCHED;
;             PG8_LDA(At, 1, 1); PG8_STAGE(PG8_SB(1, 0), b3, voffB); PG8_STAGE(PG8_SB(1, 1), b3 + hstepB, voffB); PG8_STAGE(PG8_SA(1, 0), a3, voffA);
	s_add_i32 s33, 0, 0x18000
	s_add_i32 s80, 0, 0x1c000
	v_add_u32_e32 v12, s33, v211
	v_add_u32_e32 v28, s80, v211
	ds_read_b128 v[0:3], v12
	ds_read_b128 v[4:7], v12 offset:1024
	ds_read_b128 v[8:11], v12 offset:2048
	ds_read_b128 v[12:15], v12 offset:3072
	ds_read_b128 v[16:19], v28
	ds_read_b128 v[20:23], v28 offset:1024
	ds_read_b128 v[24:27], v28 offset:2048
	ds_read_b128 v[28:31], v28 offset:3072
	s_add_u32 s0, s78, s18
	s_addc_u32 s1, s79, s19
	s_mov_b32 m0, s86
	v_lshl_add_u64 v[180:181], s[0:1], 0, v[184:185]
	ds_read_b128 v[172:175], v217 offset:32768
	ds_read_b128 v[176:179], v217 offset:33792
	ds_read_b128 v[226:229], v217 offset:34816
	ds_read_b128 v[230:233], v217 offset:35840
	ds_read_b128 v[234:237], v217 offset:36864
	ds_read_b128 v[238:241], v217 offset:37888
	ds_read_b128 v[242:245], v217 offset:38912
	ds_read_b128 v[246:249], v217 offset:39936
	s_mov_b32 m0, s71
	s_nop 0
	global_load_lds_dwordx4 v[168:169], off
	s_mov_b32 m0, s73
	s_nop 0
	global_load_lds_dwordx4 v[170:171], off
	s_mov_b32 m0, s86
	s_nop 0
	global_load_lds_dwordx4 v[180:181], off
	v_lshl_add_u64 v[180:181], s[0:1], 0, v[188:189]
	s_mov_b32 m0, s87
	s_nop 0
	global_load_lds_dwordx4 v[180:181], off
	s_waitcnt vmcnt(8)
	s_waitcnt lgkmcnt(0)
	s_barrier
	s_setprio 1
	s_waitcnt lgkmcnt(0)
	v_mfma_scale_f32_16x16x128_f8f6f4 v[164:167], v[0:7], v[172:179], v[164:167], v218, v219 op_sel_hi:[0,0,0]
	v_mfma_scale_f32_16x16x128_f8f6f4 v[160:163], v[8:15], v[172:179], v[160:163], v218, v219 op_sel_hi:[0,0,0]
	v_mfma_scale_f32_16x16x128_f8f6f4 v[140:143], v[0:7], v[226:233], v[140:143], v218, v219 op_sel_hi:[0,0,0]
	v_mfma_scale_f32_16x16x128_f8f6f4 v[136:139], v[8:15], v[226:233], v[136:139], v218, v219 op_sel_hi:[0,0,0]
	v_mfma_scale_f32_16x16x128_f8f6f4 v[108:111], v[0:7], v[234:241], v[108:111], v218, v219 op_sel_hi:[0,0,0]
	v_mfma_scale_f32_16x16x128_f8f6f4 v[104:107], v[8:15], v[234:241], v[104:107], v218, v219 op_sel_hi:[0,0,0]
	v_mfma_scale_f32_16x16x128_f8f6f4 v[116:119], v[0:7], v[242:249], v[116:119], v218, v219 op_sel_hi:[0,0,0]
	v_mfma_scale_f32_16x16x128_f8f6f4 v[112:115], v[8:15], v[242:249], v[112:115], v218, v219 op_sel_hi:[0,0,0]
	v_mfma_scale_f32_16x16x128_f8f6f4 v[148:151], v[16:23], v[172:179], v[148:151], v218, v219 op_sel_hi:[0,0,0]
	v_mfma_scale_f32_16x16x128_f8f6f4 v[144:147], v[24:31], v[172:179], v[144:147], v218, v219 op_sel_hi:[0,0,0]
	v_mfma_scale_f32_16x16x128_f8f6f4 v[132:135], v[16:23], v[226:233], v[132:135], v218, v219 op_sel_hi:[0,0,0]
	v_mfma_scale_f32_16x16x128_f8f6f4 v[128:131], v[24:31], v[226:233], v[128:131], v218, v219 op_sel_hi:[0,0,0]
	v_mfma_scale_f32_16x16x128_f8f6f4 v[124:127], v[16:23], v[234:241], v[124:127], v218, v219 op_sel_hi:[0,0,0]
	v_mfma_scale_f32_16x16x128_f8f6f4 v[120:123], v[24:31], v[234:241], v[120:123], v218, v219 op_sel_hi:[0,0,0]
	v_mfma_scale_f32_16x16x128_f8f6f4 v[100:103], v[16:23], v[242:249], v[100:103], v218, v219 op_sel_hi:[0,0,0]
	v_mfma_scale_f32_16x16x128_f8f6f4 v[96:99], v[24:31], v[242:249], v[96:99], v218, v219 op_sel_hi:[0,0,0]
	s_setprio 0
	s_barrier
	s_add_i32 s0, s33, s45
	s_add_i32 m0, s0, 0xffffff80
	ds_read_b128 v[172:175], v217 offset:49152
	ds_read_b128 v[176:179], v217 offset:50176
	ds_read_b128 v[226:229], v217 offset:51200
	ds_read_b128 v[230:233], v217 offset:52224
	ds_read_b128 v[234:237], v217 offset:53248
	ds_read_b128 v[238:241], v217 offset:54272
	ds_read_b128 v[242:245], v217 offset:55296
	ds_read_b128 v[246:249], v217 offset:56320
	global_load_lds_dwordx4 v[152:153], off offset:128
	s_add_i32 m0, s0, 0x1f80
	s_add_i32 s0, s80, s45
	global_load_lds_dwordx4 v[154:155], off offset:128
	s_add_i32 m0, s0, 0xffffff80
	s_nop 0
	global_load_lds_dwordx4 v[156:157], off offset:128
	s_add_i32 m0, s0, 0x1f80
	s_nop 0
	global_load_lds_dwordx4 v[158:159], off offset:128
	s_cmp_ge_i32 s83, s91
	s_cbranch_scc0 .Lkr6_b
	s_add_i32 m0, s93, 0xffffff80
	s_nop 0
	global_load_lds_dwordx4 v[168:169], off offset:128
	s_add_i32 m0, s94, 0xffffff80
	s_nop 0
	global_load_lds_dwordx4 v[170:171], off offset:128
